# mix GEMM: mid-hook ai=0 gate-logit loads issued before the first K segment into loop-free registers (first unit), mid hook starts with register moves
# speedup vs baseline: 1.0050x; 1.0008x over previous
.LBB0_1036:
	s_add_u32 s14, s74, 0x11800000
	s_addc_u32 s15, s75, 0
	s_add_u32 s16, s74, 0x13800000
	s_addc_u32 s17, s75, 0
	v_and_b32_e32 v170, 3, v1
	s_add_u32 s18, s74, 0x17800000
	v_and_b32_e32 v169, 15, v0
	v_lshlrev_b32_e32 v4, 4, v170
	v_lshlrev_b32_e32 v6, 2, v0
	s_sext_i32_i8 s2, s4
	s_addc_u32 s19, s75, 0
	v_lshl_or_b32 v5, v169, 6, v4
	s_lshl_b32 s4, s5, 13
	v_and_b32_e32 v6, 32, v6
	v_bitop3_b32 v5, v5, s4, v6 bitop3:0xde
	s_lshl_b32 s4, s20, 5
	s_and_b32 s91, s4, 0x60
	v_lshlrev_b32_e32 v7, 6, v0
	s_movk_i32 s4, 0x3c0
	s_lshl_b32 s87, s5, 6
	v_and_or_b32 v4, v7, s4, v4
	s_lshl_b32 s4, s91, 7
	v_bitop3_b32 v4, s4, v4, v6 bitop3:0xf6
	s_add_u32 s4, s62, 0x80
	s_waitcnt vmcnt(2)
	s_barrier
	s_addc_u32 s5, s63, 0
	s_add_i32 s92, s79, 0x18000
	s_mov_b32 s20, m0
	s_mov_b32 m0, s92
	s_nop 2
	global_load_lds_dwordx4 v166, s[4:5]
	s_mov_b32 m0, s20
	s_add_i32 s93, s79, 0x1a000
	s_mov_b32 s20, m0
	s_mov_b32 m0, s93
	s_nop 2
	global_load_lds_dwordx4 v168, s[4:5]
	s_mov_b32 m0, s20
	s_add_u32 s4, s64, 0x80
	s_addc_u32 s5, s65, 0
	s_add_i32 s94, s79, 0x8000
	s_mov_b32 s20, m0
	s_mov_b32 m0, s94
	s_nop 2
	global_load_lds_dwordx4 v165, s[4:5]
	s_mov_b32 m0, s20
	s_add_i32 s95, s79, 0xa000
	s_mov_b32 s20, m0
	s_mov_b32 m0, s95
	s_nop 2
	global_load_lds_dwordx4 v167, s[4:5]
	s_mov_b32 m0, s20
	s_add_u32 s4, s62, 0x40080
	s_addc_u32 s5, s63, 0
	s_add_i32 s96, s79, 0x1c000
	s_mov_b32 s20, m0
	s_mov_b32 m0, s96
	s_nop 2
	global_load_lds_dwordx4 v166, s[4:5]
	s_mov_b32 m0, s20
	v_or_b32_e32 v2, s87, v169
	s_add_i32 s97, s79, 0x1e000
	s_mov_b32 s20, m0
	s_mov_b32 m0, s97
	s_nop 2
	global_load_lds_dwordx4 v168, s[4:5]
	s_mov_b32 m0, s20
	v_lshlrev_b32_e32 v3, 3, v170
	s_waitcnt vmcnt(6)
	s_add_i32 s26, s79, 0xc000
	v_lshlrev_b32_e32 v2, 10, v2
	s_cmpk_lt_u32 s3, 0x100
	v_or3_b32 v171, v3, v2, s91
	v_add_u32_e32 v2, 0, v4
	s_cselect_b64 s[20:21], -1, 0
	s_add_i32 s27, s79, 0xe000
	s_ashr_i32 s34, s90, 31
	v_mov_b64_e32 v[130:131], 0x100
	v_mov_b64_e32 v[132:133], 0xff
	v_add_u32_e32 v172, 0x10000, v2
	v_add_u32_e32 v173, 0x14000, v2
	v_add_u32_e32 v174, 0, v5
	v_add_u32_e32 v175, 0x18000, v2
	v_add_u32_e32 v176, 0x1c000, v2
	s_mov_b32 s35, 0xc2a00000
	v_mov_b32_e32 v135, 0
	v_mov_b32_e32 v177, 0x42a00000
	s_lshl_b32 s32, s2, 16
	s_lshl_b32 s37, s60, 18
	s_add_i32 s32, s32, s37
	v_lshrrev_b32_e32 v214, 6, v0
	v_lshlrev_b32_e32 v214, 13, v214
	v_and_b32_e32 v215, 63, v0
	v_lshl_add_u32 v214, v215, 3, v214
	v_add_u32_e32 v252, s32, v214
	global_load_dwordx2 v[220:221], v252, s[14:15]
	global_load_dwordx2 v[222:223], v252, s[16:17]
	global_load_dwordx2 v[224:225], v252, s[14:15] offset:512
	global_load_dwordx2 v[226:227], v252, s[16:17] offset:512
	global_load_dwordx2 v[228:229], v252, s[14:15] offset:1024
	global_load_dwordx2 v[230:231], v252, s[16:17] offset:1024
	global_load_dwordx2 v[232:233], v252, s[14:15] offset:1536
	global_load_dwordx2 v[234:235], v252, s[16:17] offset:1536
	global_load_dwordx2 v[236:237], v252, s[14:15] offset:2048
	global_load_dwordx2 v[238:239], v252, s[16:17] offset:2048
	global_load_dwordx2 v[240:241], v252, s[14:15] offset:2560
	global_load_dwordx2 v[242:243], v252, s[16:17] offset:2560
	global_load_dwordx2 v[244:245], v252, s[14:15] offset:3072
	global_load_dwordx2 v[246:247], v252, s[16:17] offset:3072
	global_load_dwordx2 v[248:249], v252, s[14:15] offset:3584
	global_load_dwordx2 v[250:251], v252, s[16:17] offset:3584
	s_mov_b32 s37, 1
	s_barrier
	s_branch .LBB0_1039

.LBB0_1038:
	s_mov_b32 s37, 0
	s_andn2_b64 vcc, exec, s[4:5]
	s_mov_b32 s60, s54
	s_mov_b32 s2, s22
	s_mov_b64 s[62:63], s[58:59]
	s_mov_b64 s[64:65], s[56:57]
	s_cbranch_vccz .LBB0_1054

.Lmid1046:
	ds_read_b128 v[136:139], v175
	ds_read_b128 v[140:143], v175 offset:1024
	ds_read_b128 v[144:147], v175 offset:2048
	ds_read_b128 v[148:151], v175 offset:3072
	ds_read_b128 v[152:155], v176
	ds_read_b128 v[156:159], v176 offset:1024
	ds_read_b128 v[160:163], v176 offset:2048
	ds_read_b128 v[178:181], v176 offset:3072
	ds_read_b128 v[182:185], v174 offset:32768
	ds_read_b128 v[186:189], v174 offset:33792
	ds_read_b128 v[190:193], v174 offset:34816
	ds_read_b128 v[194:197], v174 offset:35840
	ds_read_b128 v[198:201], v174 offset:36864
	ds_read_b128 v[202:205], v174 offset:37888
	ds_read_b128 v[206:209], v174 offset:38912
	ds_read_b128 v[210:213], v174 offset:39936
	s_add_u32 s28, s25, 0x40100
	s_addc_u32 s29, s33, 0
	s_mov_b32 s25, m0
	s_mov_b32 m0, s85
	s_nop 2
	global_load_lds_dwordx4 v165, s[28:29]
	s_mov_b32 m0, s25
	s_nop 0
	s_mov_b32 s25, m0
	s_mov_b32 m0, s86
	s_nop 2
	global_load_lds_dwordx4 v167, s[28:29]
	s_mov_b32 m0, s25
	s_waitcnt vmcnt(8)
	s_waitcnt lgkmcnt(0)
	s_barrier
	s_setprio 1
	s_waitcnt lgkmcnt(7)
	v_mfma_f32_16x16x32_bf16 v[26:29], v[136:139], v[182:185], v[26:29]
	v_mfma_f32_16x16x32_bf16 v[30:33], v[144:147], v[182:185], v[30:33]
	s_waitcnt lgkmcnt(5)
	v_mfma_f32_16x16x32_bf16 v[50:53], v[136:139], v[190:193], v[50:53]
	v_mfma_f32_16x16x32_bf16 v[54:57], v[144:147], v[190:193], v[54:57]
	s_waitcnt lgkmcnt(3)
	v_mfma_f32_16x16x32_bf16 v[74:77], v[136:139], v[198:201], v[74:77]
	v_mfma_f32_16x16x32_bf16 v[78:81], v[144:147], v[198:201], v[78:81]
	s_waitcnt lgkmcnt(1)
	v_mfma_f32_16x16x32_bf16 v[94:97], v[136:139], v[206:209], v[94:97]
	v_mfma_f32_16x16x32_bf16 v[102:105], v[144:147], v[206:209], v[102:105]
	v_mfma_f32_16x16x32_bf16 v[26:29], v[140:143], v[186:189], v[26:29]
	v_mfma_f32_16x16x32_bf16 v[30:33], v[148:151], v[186:189], v[30:33]
	v_mfma_f32_16x16x32_bf16 v[50:53], v[140:143], v[194:197], v[50:53]
	v_mfma_f32_16x16x32_bf16 v[54:57], v[148:151], v[194:197], v[54:57]
	v_mfma_f32_16x16x32_bf16 v[74:77], v[140:143], v[202:205], v[74:77]
	v_mfma_f32_16x16x32_bf16 v[78:81], v[148:151], v[202:205], v[78:81]
	s_waitcnt lgkmcnt(0)
	v_mfma_f32_16x16x32_bf16 v[94:97], v[140:143], v[210:213], v[94:97]
	v_mfma_f32_16x16x32_bf16 v[102:105], v[148:151], v[210:213], v[102:105]
	s_setprio 0
	s_setprio 1
	v_mfma_f32_16x16x32_bf16 v[38:41], v[152:155], v[182:185], v[38:41]
	v_mfma_f32_16x16x32_bf16 v[42:45], v[160:163], v[182:185], v[42:45]
	v_mfma_f32_16x16x32_bf16 v[62:65], v[152:155], v[190:193], v[62:65]
	v_mfma_f32_16x16x32_bf16 v[66:69], v[160:163], v[190:193], v[66:69]
	v_mfma_f32_16x16x32_bf16 v[82:85], v[152:155], v[198:201], v[82:85]
	v_mfma_f32_16x16x32_bf16 v[90:93], v[160:163], v[198:201], v[90:93]
	v_mfma_f32_16x16x32_bf16 v[106:109], v[152:155], v[206:209], v[106:109]
	v_mfma_f32_16x16x32_bf16 v[114:117], v[160:163], v[206:209], v[114:117]
	v_mfma_f32_16x16x32_bf16 v[38:41], v[156:159], v[186:189], v[38:41]
	v_mfma_f32_16x16x32_bf16 v[42:45], v[178:181], v[186:189], v[42:45]
	v_mfma_f32_16x16x32_bf16 v[62:65], v[156:159], v[194:197], v[62:65]
	v_mfma_f32_16x16x32_bf16 v[66:69], v[178:181], v[194:197], v[66:69]
	v_mfma_f32_16x16x32_bf16 v[82:85], v[156:159], v[202:205], v[82:85]
	v_mfma_f32_16x16x32_bf16 v[90:93], v[178:181], v[202:205], v[90:93]
	v_mfma_f32_16x16x32_bf16 v[106:109], v[156:159], v[210:213], v[106:109]
	v_mfma_f32_16x16x32_bf16 v[114:117], v[178:181], v[210:213], v[114:117]
	s_setprio 0
	s_barrier
	ds_read_b128 v[182:185], v174 offset:49152
	ds_read_b128 v[186:189], v174 offset:50176
	ds_read_b128 v[190:193], v174 offset:51200
	ds_read_b128 v[194:197], v174 offset:52224
	ds_read_b128 v[198:201], v174 offset:53248
	ds_read_b128 v[202:205], v174 offset:54272
	ds_read_b128 v[206:209], v174 offset:55296
	ds_read_b128 v[210:213], v174 offset:56320
	s_add_u32 s28, s23, 0x180
	s_addc_u32 s29, s24, 0
	s_mov_b32 s25, m0
	s_mov_b32 m0, s92
	s_nop 2
	global_load_lds_dwordx4 v166, s[28:29]
	s_mov_b32 m0, s25
	s_nop 0
	s_mov_b32 s25, m0
	s_mov_b32 m0, s93
	s_nop 2
	global_load_lds_dwordx4 v168, s[28:29]
	s_mov_b32 m0, s25
	s_add_u32 s28, s23, 0x40180
	s_addc_u32 s29, s24, 0
	s_mov_b32 s23, m0
	s_mov_b32 m0, s96
	s_nop 2
	global_load_lds_dwordx4 v166, s[28:29]
	s_mov_b32 m0, s23
	s_nop 0
	s_mov_b32 s23, m0
	s_mov_b32 m0, s97
	s_nop 2
	global_load_lds_dwordx4 v168, s[28:29]
	s_mov_b32 m0, s23
	s_nop 0
	s_mov_b32 s23, m0
	s_mov_b32 m0, s94
	s_nop 2
	global_load_lds_dwordx4 v165, s[58:59]
	s_mov_b32 m0, s23
	s_nop 0
	s_mov_b32 s23, m0
	s_mov_b32 m0, s95
	s_nop 2
	global_load_lds_dwordx4 v167, s[58:59]
	s_mov_b32 m0, s23
	s_waitcnt vmcnt(8)
	s_waitcnt lgkmcnt(0)
	s_barrier
	s_setprio 1
	s_waitcnt lgkmcnt(7)
	v_mfma_f32_16x16x32_bf16 v[118:121], v[136:139], v[182:185], v[118:121]
	v_mfma_f32_16x16x32_bf16 v[126:129], v[144:147], v[182:185], v[126:129]
	s_waitcnt lgkmcnt(5)
	v_mfma_f32_16x16x32_bf16 v[98:101], v[136:139], v[190:193], v[98:101]
	v_mfma_f32_16x16x32_bf16 v[86:89], v[144:147], v[190:193], v[86:89]
	s_waitcnt lgkmcnt(3)
	v_mfma_f32_16x16x32_bf16 v[46:49], v[136:139], v[198:201], v[46:49]
	v_mfma_f32_16x16x32_bf16 v[34:37], v[144:147], v[198:201], v[34:37]
	s_waitcnt lgkmcnt(1)
	v_mfma_f32_16x16x32_bf16 v[14:17], v[136:139], v[206:209], v[14:17]
	v_mfma_f32_16x16x32_bf16 v[10:13], v[144:147], v[206:209], v[10:13]
	v_mfma_f32_16x16x32_bf16 v[118:121], v[140:143], v[186:189], v[118:121]
	v_mfma_f32_16x16x32_bf16 v[126:129], v[148:151], v[186:189], v[126:129]
	v_mfma_f32_16x16x32_bf16 v[98:101], v[140:143], v[194:197], v[98:101]
	v_mfma_f32_16x16x32_bf16 v[86:89], v[148:151], v[194:197], v[86:89]
	v_mfma_f32_16x16x32_bf16 v[46:49], v[140:143], v[202:205], v[46:49]
	v_mfma_f32_16x16x32_bf16 v[34:37], v[148:151], v[202:205], v[34:37]
	s_waitcnt lgkmcnt(0)
	v_mfma_f32_16x16x32_bf16 v[14:17], v[140:143], v[210:213], v[14:17]
	v_mfma_f32_16x16x32_bf16 v[10:13], v[148:151], v[210:213], v[10:13]
	s_setprio 0
	s_setprio 1
	v_mfma_f32_16x16x32_bf16 v[122:125], v[152:155], v[182:185], v[122:125]
	v_mfma_f32_16x16x32_bf16 v[110:113], v[160:163], v[182:185], v[110:113]
	v_mfma_f32_16x16x32_bf16 v[70:73], v[152:155], v[190:193], v[70:73]
	v_mfma_f32_16x16x32_bf16 v[58:61], v[160:163], v[190:193], v[58:61]
	v_mfma_f32_16x16x32_bf16 v[22:25], v[152:155], v[198:201], v[22:25]
	v_mfma_f32_16x16x32_bf16 v[18:21], v[160:163], v[198:201], v[18:21]
	v_mfma_f32_16x16x32_bf16 v[6:9], v[152:155], v[206:209], v[6:9]
	v_mfma_f32_16x16x32_bf16 v[2:5], v[160:163], v[206:209], v[2:5]
	v_mfma_f32_16x16x32_bf16 v[122:125], v[156:159], v[186:189], v[122:125]
	v_mfma_f32_16x16x32_bf16 v[110:113], v[178:181], v[186:189], v[110:113]
	v_mfma_f32_16x16x32_bf16 v[70:73], v[156:159], v[194:197], v[70:73]
	v_mfma_f32_16x16x32_bf16 v[58:61], v[178:181], v[194:197], v[58:61]
	v_mfma_f32_16x16x32_bf16 v[22:25], v[156:159], v[202:205], v[22:25]
	v_mfma_f32_16x16x32_bf16 v[18:21], v[178:181], v[202:205], v[18:21]
	v_mfma_f32_16x16x32_bf16 v[6:9], v[156:159], v[210:213], v[6:9]
	v_mfma_f32_16x16x32_bf16 v[2:5], v[178:181], v[210:213], v[2:5]
	s_setprio 0
	s_barrier
	s_add_i32 s3, s3, 2
	s_add_u32 s56, s56, 0x100
	s_addc_u32 s57, s57, 0
	s_cmp_gt_u32 s3, 5
	s_cbranch_scc0 .LBB0_1046
	s_ashr_i32 s55, s54, 31
	s_lshl_b64 s[24:25], s[54:55], 19
	s_add_u32 s56, s69, s24
	s_addc_u32 s57, s76, s25
	s_ashr_i32 s23, s22, 31
	s_lshl_b64 s[24:25], s[22:23], 19
	s_add_u32 s58, s77, s24
	s_addc_u32 s59, s78, s25
	s_lshl_b32 s3, s60, 18
	s_lshl_b32 s23, s2, 8
	s_lshl_b32 s32, s2, 16
	s_add_i32 s2, s32, s3
	v_lshrrev_b32_e32 v214, 6, v0
	v_lshlrev_b32_e32 v214, 13, v214
	v_and_b32_e32 v215, 63, v0
	v_lshl_add_u32 v214, v215, 3, v214
	v_add_u32_e32 v134, s2, v214
	s_cmp_lg_u32 s37, 0
	s_cbranch_scc1 .Lmpf_have
	global_load_dwordx2 v[162:163], v134, s[14:15]
	global_load_dwordx2 v[178:179], v134, s[16:17]
	v_or_b32_e32 v136, 0x200, v134
	v_add_u32_e32 v137, 0x400, v134
	v_add_u32_e32 v138, 0x600, v134
	v_add_u32_e32 v139, 0x800, v134
	v_add_u32_e32 v140, 0xa00, v134
	v_add_u32_e32 v141, 0xc00, v134
	v_add_u32_e32 v161, 0xe00, v134
	global_load_dwordx2 v[180:181], v136, s[14:15]
	global_load_dwordx2 v[182:183], v136, s[16:17]
	global_load_dwordx2 v[158:159], v137, s[14:15]
	global_load_dwordx2 v[156:157], v137, s[16:17]
	global_load_dwordx2 v[154:155], v138, s[14:15]
	global_load_dwordx2 v[152:153], v138, s[16:17]
	global_load_dwordx2 v[150:151], v139, s[14:15]
	global_load_dwordx2 v[148:149], v139, s[16:17]
	global_load_dwordx2 v[146:147], v140, s[14:15]
	global_load_dwordx2 v[144:145], v140, s[16:17]
	global_load_dwordx2 v[142:143], v141, s[14:15]
	s_nop 0
	global_load_dwordx2 v[140:141], v141, s[16:17]
	s_nop 0
	global_load_dwordx2 v[138:139], v161, s[14:15]
	global_load_dwordx2 v[136:137], v161, s[16:17]
	s_branch .Lmpf_join
.Lmpf_have:
	v_mov_b64_e32 v[162:163], v[220:221]
	v_mov_b64_e32 v[178:179], v[222:223]
	v_mov_b64_e32 v[180:181], v[224:225]
	v_mov_b64_e32 v[182:183], v[226:227]
	v_mov_b64_e32 v[158:159], v[228:229]
	v_mov_b64_e32 v[156:157], v[230:231]
	v_mov_b64_e32 v[154:155], v[232:233]
	v_mov_b64_e32 v[152:153], v[234:235]
	v_mov_b64_e32 v[150:151], v[236:237]
	v_mov_b64_e32 v[148:149], v[238:239]
	v_mov_b64_e32 v[146:147], v[240:241]
	v_mov_b64_e32 v[144:145], v[242:243]
	v_mov_b64_e32 v[142:143], v[244:245]
	v_mov_b64_e32 v[140:141], v[246:247]
	v_mov_b64_e32 v[138:139], v[248:249]
	v_mov_b64_e32 v[136:137], v[250:251]
.Lmpf_join:
	v_add_u32_e32 v160, 0x1000, v134
	global_load_dwordx2 v[220:221], v160, s[14:15]
	global_load_dwordx2 v[222:223], v160, s[16:17]
	v_add_u32_e32 v219, 0x1200, v134
	v_add_u32_e32 v215, 0x1400, v134
	v_add_u32_e32 v216, 0x1600, v134
	v_add_u32_e32 v217, 0x1800, v134
	global_load_dwordx2 v[224:225], v219, s[14:15]
	global_load_dwordx2 v[226:227], v219, s[16:17]
	global_load_dwordx2 v[228:229], v215, s[14:15]
	global_load_dwordx2 v[230:231], v215, s[16:17]
	global_load_dwordx2 v[232:233], v216, s[14:15]
	global_load_dwordx2 v[234:235], v216, s[16:17]
	global_load_dwordx2 v[236:237], v217, s[14:15]
	global_load_dwordx2 v[238:239], v217, s[16:17]
	v_add_u32_e32 v219, 0x1a00, v134
	v_add_u32_e32 v215, 0x1c00, v134
	v_add_u32_e32 v216, 0x1e00, v134
	global_load_dwordx2 v[240:241], v219, s[14:15]
	global_load_dwordx2 v[242:243], v219, s[16:17]
	global_load_dwordx2 v[244:245], v215, s[14:15]
	global_load_dwordx2 v[246:247], v215, s[16:17]
	global_load_dwordx2 v[248:249], v216, s[14:15]
	global_load_dwordx2 v[250:251], v216, s[16:17]
	s_and_b64 s[2:3], s[4:5], exec
	s_cselect_b32 s2, s57, s65
	s_cselect_b32 s3, s56, s64
	s_cselect_b32 s24, s59, s63
	s_cselect_b32 s25, s58, s62
	s_add_u32 s28, s64, 0x500
	s_addc_u32 s29, s65, 0
	s_add_u32 s30, s62, 0x500
	s_addc_u32 s31, s63, 0
	s_mov_b32 s33, 6
	s_waitcnt vmcnt(31)
	v_cvt_pk_f32_fp8_e32 v[184:185], v162
	s_waitcnt vmcnt(30)
	v_cvt_pk_f32_fp8_e32 v[190:191], v178
	v_cvt_pk_f32_fp8_e32 v[188:189], v163
	v_cvt_pk_f32_fp8_sdwa v[192:193], v178 src0_sel:WORD_1
	v_cvt_pk_f32_fp8_e32 v[194:195], v179
	v_max_f32_e32 v161, v190, v190
	v_max_f32_e32 v190, v191, v191
	v_med3_f32 v161, v161, s35, v177
	v_med3_f32 v184, v184, s35, v177
	v_max_f32_e32 v191, v192, v192
	v_max_f32_e32 v192, v193, v193
	v_max_f32_e32 v193, v194, v194
	v_max_f32_e32 v194, v195, v195
	v_med3_f32 v190, v190, s35, v177
	v_med3_f32 v185, v185, s35, v177
	v_med3_f32 v188, v188, s35, v177
	v_mul_f32_e32 v161, 0xbfb8aa3b, v161
	v_mul_f32_e32 v195, 0xbfb8aa3b, v184
	v_cvt_pk_f32_fp8_sdwa v[186:187], v162 src0_sel:WORD_1
	v_cvt_pk_f32_fp8_sdwa v[162:163], v163 src0_sel:WORD_1
	v_med3_f32 v194, v194, s35, v177
	v_med3_f32 v189, v189, s35, v177
	v_mul_f32_e32 v190, 0xbfb8aa3b, v190
	v_mul_f32_e32 v196, 0xbfb8aa3b, v185
	v_mul_f32_e32 v199, 0xbfb8aa3b, v188
	v_exp_f32_e32 v184, v161
	v_exp_f32_e32 v161, v195
	v_mul_f32_e32 v200, 0xbfb8aa3b, v194
	v_mul_f32_e32 v189, 0xbfb8aa3b, v189
	v_exp_f32_e32 v185, v190
	v_exp_f32_e32 v190, v196
	v_exp_f32_e32 v194, v199
	v_exp_f32_e32 v195, v189
	v_cvt_pk_f32_fp8_sdwa v[178:179], v179 src0_sel:WORD_1
	v_add_f32_e32 v161, 1.0, v161
	v_add_f32_e32 v189, 1.0, v190
	v_rcp_f32_e32 v190, v161
	v_add_f32_e32 v161, 1.0, v194
	v_med3_f32 v162, v162, s35, v177
	v_rcp_f32_e32 v194, v161
	v_add_f32_e32 v161, 1.0, v195
	v_mul_f32_e32 v162, 0xbfb8aa3b, v162
	v_rcp_f32_e32 v195, v161
	v_max_f32_e32 v161, v178, v178
	v_exp_f32_e32 v178, v162
	v_med3_f32 v161, v161, s35, v177
	v_med3_f32 v163, v163, s35, v177
	v_mul_f32_e32 v161, 0xbfb8aa3b, v161
	v_mul_f32_e32 v163, 0xbfb8aa3b, v163
	v_exp_f32_e32 v162, v161
	v_add_f32_e32 v161, 1.0, v178
	v_max_f32_e32 v178, v179, v179
	v_exp_f32_e32 v179, v163
	v_med3_f32 v191, v191, s35, v177
	v_med3_f32 v186, v186, s35, v177
	v_med3_f32 v192, v192, s35, v177
	v_med3_f32 v187, v187, s35, v177
	v_mul_f32_e32 v191, 0xbfb8aa3b, v191
	v_mul_f32_e32 v197, 0xbfb8aa3b, v186
	v_mul_f32_e32 v192, 0xbfb8aa3b, v192
	v_mul_f32_e32 v198, 0xbfb8aa3b, v187
	v_med3_f32 v178, v178, s35, v177
	v_exp_f32_e32 v186, v191
	v_exp_f32_e32 v191, v197
	v_exp_f32_e32 v187, v192
	v_exp_f32_e32 v192, v198
	v_mul_f32_e32 v163, 0xbfb8aa3b, v178
	v_exp_f32_e32 v163, v163
	v_rcp_f32_e32 v178, v161
	v_add_f32_e32 v161, 1.0, v179
	v_med3_f32 v193, v193, s35, v177
	v_rcp_f32_e32 v179, v161
	v_mul_f32_e32 v193, 0xbfb8aa3b, v193
	v_exp_f32_e32 v188, v193
	v_add_f32_e32 v193, 1.0, v191
	v_add_f32_e32 v196, 1.0, v192
	v_rcp_f32_e32 v192, v193
	v_rcp_f32_e32 v193, v196
	v_pk_add_f32 v[162:163], v[162:163], 1.0 op_sel_hi:[1,0]
	v_pk_add_f32 v[186:187], v[186:187], 1.0 op_sel_hi:[1,0]
	v_pk_mul_f32 v[162:163], v[178:179], v[162:163]
	v_pk_mul_f32 v[186:187], v[192:193], v[186:187]
	v_pk_mul_f32 v[32:33], v[32:33], v[162:163]
	s_waitcnt vmcnt(29)
	v_cvt_pk_f32_fp8_e32 v[162:163], v180
	v_pk_mul_f32 v[28:29], v[28:29], v[186:187]
	s_waitcnt vmcnt(28)
	v_cvt_pk_f32_fp8_e32 v[186:187], v182
	v_rcp_f32_e32 v191, v189
	v_med3_f32 v162, v162, s35, v177
	v_mul_f32_e32 v162, 0xbfb8aa3b, v162
	v_max_f32_e32 v161, v186, v186
	v_exp_f32_e32 v186, v162
	v_exp_f32_e32 v189, v200
	v_med3_f32 v161, v161, s35, v177
	v_cvt_pk_f32_fp8_sdwa v[178:179], v180 src0_sel:WORD_1
	v_mul_f32_e32 v161, 0xbfb8aa3b, v161
	v_med3_f32 v163, v163, s35, v177
	v_pk_add_f32 v[184:185], v[184:185], 1.0 op_sel_hi:[1,0]
	v_exp_f32_e32 v162, v161
	v_add_f32_e32 v161, 1.0, v186
	v_mul_f32_e32 v163, 0xbfb8aa3b, v163
	v_pk_mul_f32 v[184:185], v[190:191], v[184:185]
	v_rcp_f32_e32 v186, v161
	v_max_f32_e32 v161, v187, v187
	v_exp_f32_e32 v187, v163
	v_pk_mul_f32 v[26:27], v[26:27], v[184:185]
	v_pk_add_f32 v[184:185], v[188:189], 1.0 op_sel_hi:[1,0]
	v_cvt_pk_f32_fp8_sdwa v[188:189], v182 src0_sel:WORD_1
	v_med3_f32 v161, v161, s35, v177
	v_mul_f32_e32 v161, 0xbfb8aa3b, v161
	v_med3_f32 v178, v178, s35, v177
	v_exp_f32_e32 v163, v161
	v_add_f32_e32 v161, 1.0, v187
	v_mul_f32_e32 v178, 0xbfb8aa3b, v178
	v_pk_mul_f32 v[184:185], v[194:195], v[184:185]
	v_rcp_f32_e32 v187, v161
	v_max_f32_e32 v161, v188, v188
	v_exp_f32_e32 v188, v178
	v_pk_mul_f32 v[30:31], v[30:31], v[184:185]
	v_cvt_pk_f32_fp8_e32 v[184:185], v181
	v_med3_f32 v161, v161, s35, v177
	v_med3_f32 v179, v179, s35, v177
	v_mul_f32_e32 v161, 0xbfb8aa3b, v161
	v_mul_f32_e32 v179, 0xbfb8aa3b, v179
	v_pk_add_f32 v[162:163], v[162:163], 1.0 op_sel_hi:[1,0]
	v_exp_f32_e32 v178, v161
	v_add_f32_e32 v161, 1.0, v188
	v_max_f32_e32 v188, v189, v189
	v_exp_f32_e32 v189, v179
	v_pk_mul_f32 v[162:163], v[186:187], v[162:163]
	v_cvt_pk_f32_fp8_e32 v[190:191], v183
	v_pk_mul_f32 v[38:39], v[38:39], v[162:163]
	v_med3_f32 v162, v184, s35, v177
	v_med3_f32 v188, v188, s35, v177
	v_mul_f32_e32 v162, 0xbfb8aa3b, v162
	v_mul_f32_e32 v179, 0xbfb8aa3b, v188
	v_rcp_f32_e32 v188, v161
	v_add_f32_e32 v161, 1.0, v189
	v_exp_f32_e32 v163, v162
	v_exp_f32_e32 v179, v179
	v_rcp_f32_e32 v189, v161
	v_med3_f32 v161, v190, s35, v177
	v_mul_f32_e32 v161, 0xbfb8aa3b, v161
	v_exp_f32_e32 v162, v161
	v_add_f32_e32 v161, 1.0, v163
	v_cvt_pk_f32_fp8_sdwa v[180:181], v181 src0_sel:WORD_1
	v_pk_add_f32 v[178:179], v[178:179], 1.0 op_sel_hi:[1,0]
	v_med3_f32 v163, v185, s35, v177
	v_pk_mul_f32 v[178:179], v[188:189], v[178:179]
	v_mul_f32_e32 v163, 0xbfb8aa3b, v163
	v_pk_mul_f32 v[40:41], v[40:41], v[178:179]
	v_exp_f32_e32 v179, v163
	v_cvt_pk_f32_fp8_sdwa v[182:183], v183 src0_sel:WORD_1
	v_rcp_f32_e32 v178, v161
	v_med3_f32 v161, v191, s35, v177
	v_mul_f32_e32 v161, 0xbfb8aa3b, v161
	v_med3_f32 v180, v180, s35, v177
	v_exp_f32_e32 v163, v161
	v_add_f32_e32 v161, 1.0, v179
	v_mul_f32_e32 v180, 0xbfb8aa3b, v180
	v_rcp_f32_e32 v179, v161
	v_max_f32_e32 v161, v182, v182
	v_exp_f32_e32 v182, v180
	v_med3_f32 v161, v161, s35, v177
	v_med3_f32 v181, v181, s35, v177
	v_mul_f32_e32 v161, 0xbfb8aa3b, v161
	v_mul_f32_e32 v181, 0xbfb8aa3b, v181
	v_exp_f32_e32 v180, v161
	v_add_f32_e32 v161, 1.0, v182
	v_max_f32_e32 v182, v183, v183
	v_exp_f32_e32 v183, v181
	v_med3_f32 v182, v182, s35, v177
	v_mul_f32_e32 v181, 0xbfb8aa3b, v182
	v_exp_f32_e32 v181, v181
	v_rcp_f32_e32 v182, v161
	v_add_f32_e32 v161, 1.0, v183
	v_pk_add_f32 v[162:163], v[162:163], 1.0 op_sel_hi:[1,0]
	v_rcp_f32_e32 v183, v161
	v_pk_mul_f32 v[162:163], v[178:179], v[162:163]
	v_pk_add_f32 v[180:181], v[180:181], 1.0 op_sel_hi:[1,0]
	v_pk_mul_f32 v[42:43], v[42:43], v[162:163]
	s_waitcnt vmcnt(27)
	v_cvt_pk_f32_fp8_e32 v[162:163], v158
	v_pk_mul_f32 v[178:179], v[182:183], v[180:181]
	s_waitcnt vmcnt(26)
	v_cvt_pk_f32_fp8_e32 v[182:183], v156
	v_pk_mul_f32 v[44:45], v[44:45], v[178:179]
	v_med3_f32 v162, v162, s35, v177
	v_mul_f32_e32 v162, 0xbfb8aa3b, v162
	v_max_f32_e32 v161, v182, v182
	v_exp_f32_e32 v182, v162
	v_med3_f32 v161, v161, s35, v177
	v_cvt_pk_f32_fp8_sdwa v[178:179], v158 src0_sel:WORD_1
	v_mul_f32_e32 v161, 0xbfb8aa3b, v161
	v_med3_f32 v163, v163, s35, v177
	v_exp_f32_e32 v162, v161
	v_add_f32_e32 v161, 1.0, v182
	v_mul_f32_e32 v163, 0xbfb8aa3b, v163
	v_rcp_f32_e32 v182, v161
	v_max_f32_e32 v161, v183, v183
	v_exp_f32_e32 v183, v163
	v_cvt_pk_f32_fp8_sdwa v[184:185], v156 src0_sel:WORD_1
	v_med3_f32 v161, v161, s35, v177
	v_mul_f32_e32 v161, 0xbfb8aa3b, v161
	v_med3_f32 v178, v178, s35, v177
	v_exp_f32_e32 v163, v161
	v_add_f32_e32 v161, 1.0, v183
	v_mul_f32_e32 v178, 0xbfb8aa3b, v178
	v_rcp_f32_e32 v183, v161
	v_max_f32_e32 v161, v184, v184
	v_exp_f32_e32 v184, v178
	v_cvt_pk_f32_fp8_e32 v[180:181], v159
	v_med3_f32 v161, v161, s35, v177
	v_med3_f32 v179, v179, s35, v177
	v_mul_f32_e32 v161, 0xbfb8aa3b, v161
	v_mul_f32_e32 v179, 0xbfb8aa3b, v179
	v_pk_add_f32 v[162:163], v[162:163], 1.0 op_sel_hi:[1,0]
	v_cvt_pk_f32_fp8_sdwa v[158:159], v159 src0_sel:WORD_1
	v_exp_f32_e32 v178, v161
	v_add_f32_e32 v161, 1.0, v184
	v_max_f32_e32 v184, v185, v185
	v_exp_f32_e32 v185, v179
	v_pk_mul_f32 v[162:163], v[182:183], v[162:163]
	v_cvt_pk_f32_fp8_e32 v[186:187], v157
	v_pk_mul_f32 v[50:51], v[50:51], v[162:163]
	v_med3_f32 v162, v180, s35, v177
	v_med3_f32 v184, v184, s35, v177
	v_mul_f32_e32 v162, 0xbfb8aa3b, v162
	v_cvt_pk_f32_fp8_sdwa v[156:157], v157 src0_sel:WORD_1
	v_mul_f32_e32 v179, 0xbfb8aa3b, v184
	v_rcp_f32_e32 v184, v161
	v_add_f32_e32 v161, 1.0, v185
	v_exp_f32_e32 v163, v162
	v_exp_f32_e32 v179, v179
	v_rcp_f32_e32 v185, v161
	v_med3_f32 v158, v158, s35, v177
	v_med3_f32 v159, v159, s35, v177
	v_med3_f32 v161, v186, s35, v177
	v_mul_f32_e32 v158, 0xbfb8aa3b, v158
	v_mul_f32_e32 v159, 0xbfb8aa3b, v159
	v_mul_f32_e32 v161, 0xbfb8aa3b, v161
	v_exp_f32_e32 v158, v158
	v_exp_f32_e32 v159, v159
	v_exp_f32_e32 v162, v161
	v_add_f32_e32 v161, 1.0, v163
	v_pk_add_f32 v[178:179], v[178:179], 1.0 op_sel_hi:[1,0]
	v_med3_f32 v163, v181, s35, v177
	v_med3_f32 v156, v156, s35, v177
	v_med3_f32 v157, v157, s35, v177
	v_pk_mul_f32 v[178:179], v[184:185], v[178:179]
	v_mul_f32_e32 v163, 0xbfb8aa3b, v163
	v_mul_f32_e32 v156, 0xbfb8aa3b, v156
	v_mul_f32_e32 v157, 0xbfb8aa3b, v157
	v_pk_mul_f32 v[52:53], v[52:53], v[178:179]
	v_exp_f32_e32 v179, v163
	v_exp_f32_e32 v156, v156
	v_add_f32_e32 v158, 1.0, v158
	v_exp_f32_e32 v157, v157
	v_add_f32_e32 v159, 1.0, v159
	v_rcp_f32_e32 v178, v161
	v_rcp_f32_e32 v158, v158
	v_rcp_f32_e32 v159, v159
	v_med3_f32 v161, v187, s35, v177
	v_mul_f32_e32 v161, 0xbfb8aa3b, v161
	v_exp_f32_e32 v163, v161
	v_add_f32_e32 v161, 1.0, v179
	v_pk_add_f32 v[156:157], v[156:157], 1.0 op_sel_hi:[1,0]
	v_rcp_f32_e32 v179, v161
	v_pk_mul_f32 v[156:157], v[158:159], v[156:157]
	v_pk_add_f32 v[162:163], v[162:163], 1.0 op_sel_hi:[1,0]
	v_pk_mul_f32 v[56:57], v[56:57], v[156:157]
	s_waitcnt vmcnt(25)
	v_cvt_pk_f32_fp8_e32 v[156:157], v154
	v_pk_mul_f32 v[162:163], v[178:179], v[162:163]
	s_waitcnt vmcnt(24)
	v_cvt_pk_f32_fp8_e32 v[178:179], v152
	v_cvt_pk_f32_fp8_sdwa v[158:159], v154 src0_sel:WORD_1
	v_med3_f32 v156, v156, s35, v177
	v_mul_f32_e32 v156, 0xbfb8aa3b, v156
	v_max_f32_e32 v161, v178, v178
	v_exp_f32_e32 v178, v156
	v_med3_f32 v157, v157, s35, v177
	v_med3_f32 v156, v161, s35, v177
	v_add_f32_e32 v161, 1.0, v178
	v_mul_f32_e32 v157, 0xbfb8aa3b, v157
	v_rcp_f32_e32 v178, v161
	v_max_f32_e32 v161, v179, v179
	v_exp_f32_e32 v179, v157
	v_cvt_pk_f32_fp8_sdwa v[180:181], v152 src0_sel:WORD_1
	v_med3_f32 v158, v158, s35, v177
	v_med3_f32 v157, v161, s35, v177
	v_add_f32_e32 v161, 1.0, v179
	v_mul_f32_e32 v158, 0xbfb8aa3b, v158
	v_rcp_f32_e32 v179, v161
	v_max_f32_e32 v161, v180, v180
	v_exp_f32_e32 v180, v158
	v_med3_f32 v159, v159, s35, v177
	v_pk_mul_f32 v[54:55], v[54:55], v[162:163]
	v_cvt_pk_f32_fp8_e32 v[162:163], v155
	v_cvt_pk_f32_fp8_sdwa v[154:155], v155 src0_sel:WORD_1
	v_mul_f32_e32 v156, 0xbfb8aa3b, v156
	v_mul_f32_e32 v157, 0xbfb8aa3b, v157
	v_mul_f32_e32 v159, 0xbfb8aa3b, v159
	v_exp_f32_e32 v156, v156
	v_exp_f32_e32 v157, v157
	v_med3_f32 v158, v161, s35, v177
	v_add_f32_e32 v161, 1.0, v180
	v_max_f32_e32 v180, v181, v181
	v_exp_f32_e32 v181, v159
	v_med3_f32 v180, v180, s35, v177
	v_cvt_pk_f32_fp8_e32 v[182:183], v153
	v_cvt_pk_f32_fp8_sdwa v[152:153], v153 src0_sel:WORD_1
	v_mul_f32_e32 v158, 0xbfb8aa3b, v158
	v_mul_f32_e32 v159, 0xbfb8aa3b, v180
	v_exp_f32_e32 v158, v158
	v_exp_f32_e32 v159, v159
	v_rcp_f32_e32 v180, v161
	v_add_f32_e32 v161, 1.0, v181
	v_pk_add_f32 v[156:157], v[156:157], 1.0 op_sel_hi:[1,0]
	v_med3_f32 v154, v154, s35, v177
	v_med3_f32 v155, v155, s35, v177
	v_rcp_f32_e32 v181, v161
	v_pk_mul_f32 v[156:157], v[178:179], v[156:157]
	v_mul_f32_e32 v154, 0xbfb8aa3b, v154
	v_mul_f32_e32 v155, 0xbfb8aa3b, v155
	v_pk_mul_f32 v[62:63], v[62:63], v[156:157]
	v_exp_f32_e32 v154, v154
	v_exp_f32_e32 v155, v155
	v_med3_f32 v157, v162, s35, v177
	v_pk_add_f32 v[158:159], v[158:159], 1.0 op_sel_hi:[1,0]
	v_mul_f32_e32 v157, 0xbfb8aa3b, v157
	v_med3_f32 v152, v152, s35, v177
	v_med3_f32 v153, v153, s35, v177
	v_pk_mul_f32 v[158:159], v[180:181], v[158:159]
	v_exp_f32_e32 v157, v157
	v_mul_f32_e32 v152, 0xbfb8aa3b, v152
	v_mul_f32_e32 v153, 0xbfb8aa3b, v153
	v_pk_mul_f32 v[64:65], v[64:65], v[158:159]
	v_exp_f32_e32 v152, v152
	v_add_f32_e32 v154, 1.0, v154
	v_exp_f32_e32 v153, v153
	v_add_f32_e32 v155, 1.0, v155
	v_med3_f32 v159, v163, s35, v177
	v_rcp_f32_e32 v154, v154
	v_rcp_f32_e32 v155, v155
	v_mul_f32_e32 v159, 0xbfb8aa3b, v159
	v_add_f32_e32 v157, 1.0, v157
	v_exp_f32_e32 v159, v159
	v_rcp_f32_e32 v158, v157
	v_pk_add_f32 v[152:153], v[152:153], 1.0 op_sel_hi:[1,0]
	v_med3_f32 v156, v182, s35, v177
	v_med3_f32 v157, v183, s35, v177
	v_pk_mul_f32 v[152:153], v[154:155], v[152:153]
	v_mul_f32_e32 v156, 0xbfb8aa3b, v156
	v_mul_f32_e32 v157, 0xbfb8aa3b, v157
	v_pk_mul_f32 v[68:69], v[68:69], v[152:153]
	s_waitcnt vmcnt(23)
	v_cvt_pk_f32_fp8_e32 v[152:153], v150
	v_exp_f32_e32 v156, v156
	v_exp_f32_e32 v157, v157
	v_add_f32_e32 v159, 1.0, v159
	v_rcp_f32_e32 v159, v159
	v_pk_add_f32 v[156:157], v[156:157], 1.0 op_sel_hi:[1,0]
	v_med3_f32 v152, v152, s35, v177
	v_pk_mul_f32 v[156:157], v[158:159], v[156:157]
	s_waitcnt vmcnt(22)
	v_cvt_pk_f32_fp8_e32 v[158:159], v148
	v_mul_f32_e32 v152, 0xbfb8aa3b, v152
	v_exp_f32_e32 v161, v152
	v_cvt_pk_f32_fp8_sdwa v[154:155], v150 src0_sel:WORD_1
	v_med3_f32 v153, v153, s35, v177
	v_mul_f32_e32 v153, 0xbfb8aa3b, v153
	v_cvt_pk_f32_fp8_sdwa v[162:163], v148 src0_sel:WORD_1
	v_med3_f32 v152, v158, s35, v177
	v_add_f32_e32 v158, 1.0, v161
	v_exp_f32_e32 v161, v153
	v_med3_f32 v154, v154, s35, v177
	v_mul_f32_e32 v154, 0xbfb8aa3b, v154
	v_med3_f32 v153, v159, s35, v177
	v_add_f32_e32 v159, 1.0, v161
	v_max_f32_e32 v161, v162, v162
	v_exp_f32_e32 v162, v154
	v_med3_f32 v155, v155, s35, v177
	v_pk_mul_f32 v[66:67], v[66:67], v[156:157]
	v_cvt_pk_f32_fp8_e32 v[156:157], v151
	v_cvt_pk_f32_fp8_sdwa v[150:151], v151 src0_sel:WORD_1
	v_mul_f32_e32 v152, 0xbfb8aa3b, v152
	v_mul_f32_e32 v153, 0xbfb8aa3b, v153
	v_mul_f32_e32 v155, 0xbfb8aa3b, v155
	v_exp_f32_e32 v152, v152
	v_exp_f32_e32 v153, v153
	v_med3_f32 v154, v161, s35, v177
	v_add_f32_e32 v161, 1.0, v162
	v_max_f32_e32 v162, v163, v163
	v_exp_f32_e32 v163, v155
	v_rcp_f32_e32 v158, v158
	v_rcp_f32_e32 v159, v159
	v_med3_f32 v162, v162, s35, v177
	v_cvt_pk_f32_fp8_e32 v[178:179], v149
	v_cvt_pk_f32_fp8_sdwa v[148:149], v149 src0_sel:WORD_1
	v_mul_f32_e32 v154, 0xbfb8aa3b, v154
	v_mul_f32_e32 v155, 0xbfb8aa3b, v162
	v_exp_f32_e32 v154, v154
	v_exp_f32_e32 v155, v155
	v_rcp_f32_e32 v162, v161
	v_add_f32_e32 v161, 1.0, v163
	v_pk_add_f32 v[152:153], v[152:153], 1.0 op_sel_hi:[1,0]
	v_med3_f32 v150, v150, s35, v177
	v_med3_f32 v151, v151, s35, v177
	v_rcp_f32_e32 v163, v161
	v_pk_mul_f32 v[152:153], v[158:159], v[152:153]
	v_mul_f32_e32 v150, 0xbfb8aa3b, v150
	v_mul_f32_e32 v151, 0xbfb8aa3b, v151
	v_pk_mul_f32 v[74:75], v[74:75], v[152:153]
	v_exp_f32_e32 v150, v150
	v_exp_f32_e32 v151, v151
	v_med3_f32 v153, v156, s35, v177
	v_pk_add_f32 v[154:155], v[154:155], 1.0 op_sel_hi:[1,0]
	v_mul_f32_e32 v153, 0xbfb8aa3b, v153
	v_med3_f32 v148, v148, s35, v177
	v_med3_f32 v149, v149, s35, v177
	v_pk_mul_f32 v[154:155], v[162:163], v[154:155]
	v_exp_f32_e32 v153, v153
	v_mul_f32_e32 v148, 0xbfb8aa3b, v148
	v_mul_f32_e32 v149, 0xbfb8aa3b, v149
	v_pk_mul_f32 v[76:77], v[76:77], v[154:155]
	v_exp_f32_e32 v148, v148
	v_add_f32_e32 v150, 1.0, v150
	v_exp_f32_e32 v149, v149
	v_add_f32_e32 v151, 1.0, v151
	v_med3_f32 v155, v157, s35, v177
	v_rcp_f32_e32 v150, v150
	v_rcp_f32_e32 v151, v151
	v_mul_f32_e32 v155, 0xbfb8aa3b, v155
	v_add_f32_e32 v153, 1.0, v153
	v_exp_f32_e32 v155, v155
	v_rcp_f32_e32 v154, v153
	v_pk_add_f32 v[148:149], v[148:149], 1.0 op_sel_hi:[1,0]
	v_med3_f32 v152, v178, s35, v177
	v_med3_f32 v153, v179, s35, v177
	v_pk_mul_f32 v[148:149], v[150:151], v[148:149]
	v_mul_f32_e32 v152, 0xbfb8aa3b, v152
	v_mul_f32_e32 v153, 0xbfb8aa3b, v153
	v_pk_mul_f32 v[80:81], v[80:81], v[148:149]
	s_waitcnt vmcnt(21)
	v_cvt_pk_f32_fp8_e32 v[148:149], v146
	v_exp_f32_e32 v152, v152
	v_exp_f32_e32 v153, v153
	v_add_f32_e32 v155, 1.0, v155
	v_rcp_f32_e32 v155, v155
	v_pk_add_f32 v[152:153], v[152:153], 1.0 op_sel_hi:[1,0]
	v_med3_f32 v148, v148, s35, v177
	v_pk_mul_f32 v[152:153], v[154:155], v[152:153]
	s_waitcnt vmcnt(20)
	v_cvt_pk_f32_fp8_e32 v[154:155], v144
	v_mul_f32_e32 v148, 0xbfb8aa3b, v148
	v_exp_f32_e32 v161, v148
	v_cvt_pk_f32_fp8_sdwa v[150:151], v146 src0_sel:WORD_1
	v_med3_f32 v149, v149, s35, v177
	v_mul_f32_e32 v149, 0xbfb8aa3b, v149
	v_med3_f32 v148, v154, s35, v177
	v_add_f32_e32 v154, 1.0, v161
	v_exp_f32_e32 v161, v149
	v_med3_f32 v150, v150, s35, v177
	v_cvt_pk_f32_fp8_sdwa v[156:157], v144 src0_sel:WORD_1
	v_mul_f32_e32 v150, 0xbfb8aa3b, v150
	v_med3_f32 v149, v155, s35, v177
	v_add_f32_e32 v155, 1.0, v161
	v_exp_f32_e32 v161, v150
	v_med3_f32 v151, v151, s35, v177
	v_pk_mul_f32 v[78:79], v[78:79], v[152:153]
	v_cvt_pk_f32_fp8_e32 v[152:153], v147
	v_cvt_pk_f32_fp8_sdwa v[146:147], v147 src0_sel:WORD_1
	v_mul_f32_e32 v148, 0xbfb8aa3b, v148
	v_mul_f32_e32 v149, 0xbfb8aa3b, v149
	v_mul_f32_e32 v151, 0xbfb8aa3b, v151
	v_exp_f32_e32 v148, v148
	v_exp_f32_e32 v149, v149
	v_med3_f32 v150, v156, s35, v177
	v_add_f32_e32 v156, 1.0, v161
	v_exp_f32_e32 v161, v151
	v_rcp_f32_e32 v154, v154
	v_rcp_f32_e32 v155, v155
	v_med3_f32 v157, v157, s35, v177
	v_cvt_pk_f32_fp8_e32 v[158:159], v145
	v_cvt_pk_f32_fp8_sdwa v[144:145], v145 src0_sel:WORD_1
	v_mul_f32_e32 v150, 0xbfb8aa3b, v150
	v_mul_f32_e32 v151, 0xbfb8aa3b, v157
	v_exp_f32_e32 v150, v150
	v_exp_f32_e32 v151, v151
	v_add_f32_e32 v157, 1.0, v161
	v_pk_add_f32 v[148:149], v[148:149], 1.0 op_sel_hi:[1,0]
	v_med3_f32 v146, v146, s35, v177
	v_med3_f32 v147, v147, s35, v177
	v_rcp_f32_e32 v156, v156
	v_rcp_f32_e32 v157, v157
	v_pk_mul_f32 v[148:149], v[154:155], v[148:149]
	v_mul_f32_e32 v146, 0xbfb8aa3b, v146
	v_mul_f32_e32 v147, 0xbfb8aa3b, v147
	v_pk_mul_f32 v[82:83], v[82:83], v[148:149]
	v_exp_f32_e32 v146, v146
	v_exp_f32_e32 v147, v147
	v_med3_f32 v149, v152, s35, v177
	v_pk_add_f32 v[150:151], v[150:151], 1.0 op_sel_hi:[1,0]
	v_mul_f32_e32 v149, 0xbfb8aa3b, v149
	v_med3_f32 v144, v144, s35, v177
	v_med3_f32 v145, v145, s35, v177
	v_pk_mul_f32 v[150:151], v[156:157], v[150:151]
	v_exp_f32_e32 v149, v149
	v_mul_f32_e32 v144, 0xbfb8aa3b, v144
	v_mul_f32_e32 v145, 0xbfb8aa3b, v145
	v_pk_mul_f32 v[84:85], v[84:85], v[150:151]
	v_exp_f32_e32 v144, v144
	v_add_f32_e32 v146, 1.0, v146
	v_exp_f32_e32 v145, v145
	v_add_f32_e32 v147, 1.0, v147
	v_med3_f32 v151, v153, s35, v177
	v_rcp_f32_e32 v146, v146
	v_rcp_f32_e32 v147, v147
	v_mul_f32_e32 v151, 0xbfb8aa3b, v151
	v_add_f32_e32 v149, 1.0, v149
	v_exp_f32_e32 v151, v151
	v_rcp_f32_e32 v150, v149
	v_pk_add_f32 v[144:145], v[144:145], 1.0 op_sel_hi:[1,0]
	v_med3_f32 v148, v158, s35, v177
	v_med3_f32 v149, v159, s35, v177
	v_pk_mul_f32 v[144:145], v[146:147], v[144:145]
	v_mul_f32_e32 v148, 0xbfb8aa3b, v148
	v_mul_f32_e32 v149, 0xbfb8aa3b, v149
	v_pk_mul_f32 v[92:93], v[92:93], v[144:145]
	s_waitcnt vmcnt(19)
	v_cvt_pk_f32_fp8_e32 v[144:145], v142
	v_exp_f32_e32 v148, v148
	v_exp_f32_e32 v149, v149
	v_add_f32_e32 v151, 1.0, v151
	v_rcp_f32_e32 v151, v151
	v_pk_add_f32 v[148:149], v[148:149], 1.0 op_sel_hi:[1,0]
	v_med3_f32 v144, v144, s35, v177
	v_pk_mul_f32 v[148:149], v[150:151], v[148:149]
	s_waitcnt vmcnt(18)
	v_cvt_pk_f32_fp8_e32 v[150:151], v140
	v_mul_f32_e32 v144, 0xbfb8aa3b, v144
	v_exp_f32_e32 v156, v144
	v_cvt_pk_f32_fp8_sdwa v[146:147], v142 src0_sel:WORD_1
	v_med3_f32 v145, v145, s35, v177
	v_mul_f32_e32 v145, 0xbfb8aa3b, v145
	v_med3_f32 v144, v150, s35, v177
	v_add_f32_e32 v150, 1.0, v156
	v_exp_f32_e32 v156, v145
	v_med3_f32 v146, v146, s35, v177
	v_cvt_pk_f32_fp8_sdwa v[152:153], v140 src0_sel:WORD_1
	v_mul_f32_e32 v146, 0xbfb8aa3b, v146
	v_med3_f32 v145, v151, s35, v177
	v_add_f32_e32 v151, 1.0, v156
	v_exp_f32_e32 v156, v146
	v_med3_f32 v147, v147, s35, v177
	v_pk_mul_f32 v[90:91], v[90:91], v[148:149]
	v_cvt_pk_f32_fp8_e32 v[148:149], v143
	v_cvt_pk_f32_fp8_sdwa v[142:143], v143 src0_sel:WORD_1
	v_mul_f32_e32 v144, 0xbfb8aa3b, v144
	v_mul_f32_e32 v145, 0xbfb8aa3b, v145
	v_mul_f32_e32 v147, 0xbfb8aa3b, v147
	v_exp_f32_e32 v144, v144
	v_exp_f32_e32 v145, v145
	v_med3_f32 v146, v152, s35, v177
	v_add_f32_e32 v152, 1.0, v156
	v_exp_f32_e32 v156, v147
	v_rcp_f32_e32 v150, v150
	v_rcp_f32_e32 v151, v151
	v_med3_f32 v153, v153, s35, v177
	v_cvt_pk_f32_fp8_e32 v[154:155], v141
	v_cvt_pk_f32_fp8_sdwa v[140:141], v141 src0_sel:WORD_1
	v_mul_f32_e32 v146, 0xbfb8aa3b, v146
	v_mul_f32_e32 v147, 0xbfb8aa3b, v153
	v_exp_f32_e32 v146, v146
	v_exp_f32_e32 v147, v147
	v_add_f32_e32 v153, 1.0, v156
	v_pk_add_f32 v[144:145], v[144:145], 1.0 op_sel_hi:[1,0]
	v_med3_f32 v142, v142, s35, v177
	v_med3_f32 v143, v143, s35, v177
	v_rcp_f32_e32 v152, v152
	v_rcp_f32_e32 v153, v153
	v_pk_mul_f32 v[144:145], v[150:151], v[144:145]
	v_mul_f32_e32 v142, 0xbfb8aa3b, v142
	v_mul_f32_e32 v143, 0xbfb8aa3b, v143
	v_pk_mul_f32 v[94:95], v[94:95], v[144:145]
	v_exp_f32_e32 v142, v142
	v_exp_f32_e32 v143, v143
	v_med3_f32 v145, v148, s35, v177
	v_pk_add_f32 v[146:147], v[146:147], 1.0 op_sel_hi:[1,0]
	v_mul_f32_e32 v145, 0xbfb8aa3b, v145
	v_med3_f32 v140, v140, s35, v177
	v_med3_f32 v141, v141, s35, v177
	v_pk_mul_f32 v[146:147], v[152:153], v[146:147]
	v_exp_f32_e32 v145, v145
	v_mul_f32_e32 v140, 0xbfb8aa3b, v140
	v_mul_f32_e32 v141, 0xbfb8aa3b, v141
	v_pk_mul_f32 v[96:97], v[96:97], v[146:147]
	v_exp_f32_e32 v140, v140
	v_add_f32_e32 v142, 1.0, v142
	v_exp_f32_e32 v141, v141
	v_add_f32_e32 v143, 1.0, v143
	v_med3_f32 v147, v149, s35, v177
	v_rcp_f32_e32 v142, v142
	v_rcp_f32_e32 v143, v143
	v_mul_f32_e32 v147, 0xbfb8aa3b, v147
	v_add_f32_e32 v145, 1.0, v145
	v_exp_f32_e32 v147, v147
	v_rcp_f32_e32 v146, v145
	v_pk_add_f32 v[140:141], v[140:141], 1.0 op_sel_hi:[1,0]
	v_med3_f32 v144, v154, s35, v177
	v_med3_f32 v145, v155, s35, v177
	v_pk_mul_f32 v[140:141], v[142:143], v[140:141]
	v_mul_f32_e32 v144, 0xbfb8aa3b, v144
	v_mul_f32_e32 v145, 0xbfb8aa3b, v145
	v_pk_mul_f32 v[104:105], v[104:105], v[140:141]
	s_waitcnt vmcnt(17)
	v_cvt_pk_f32_fp8_e32 v[140:141], v138
	v_exp_f32_e32 v144, v144
	v_exp_f32_e32 v145, v145
	v_add_f32_e32 v147, 1.0, v147
	v_rcp_f32_e32 v147, v147
	v_pk_add_f32 v[144:145], v[144:145], 1.0 op_sel_hi:[1,0]
	v_med3_f32 v140, v140, s35, v177
	v_pk_mul_f32 v[144:145], v[146:147], v[144:145]
	s_waitcnt vmcnt(16)
	v_cvt_pk_f32_fp8_e32 v[146:147], v136
	v_mul_f32_e32 v140, 0xbfb8aa3b, v140
	v_exp_f32_e32 v152, v140
	v_cvt_pk_f32_fp8_sdwa v[142:143], v138 src0_sel:WORD_1
	v_med3_f32 v141, v141, s35, v177
	v_mul_f32_e32 v141, 0xbfb8aa3b, v141
	v_med3_f32 v140, v146, s35, v177
	v_add_f32_e32 v146, 1.0, v152
	v_exp_f32_e32 v152, v141
	v_med3_f32 v142, v142, s35, v177
	v_cvt_pk_f32_fp8_sdwa v[148:149], v136 src0_sel:WORD_1
	v_mul_f32_e32 v142, 0xbfb8aa3b, v142
	v_med3_f32 v141, v147, s35, v177
	v_add_f32_e32 v147, 1.0, v152
	v_exp_f32_e32 v152, v142
	v_med3_f32 v143, v143, s35, v177
	v_mul_f32_e32 v140, 0xbfb8aa3b, v140
	v_mul_f32_e32 v141, 0xbfb8aa3b, v141
	v_mul_f32_e32 v143, 0xbfb8aa3b, v143
	v_exp_f32_e32 v140, v140
	v_exp_f32_e32 v141, v141
	v_med3_f32 v142, v148, s35, v177
	v_add_f32_e32 v148, 1.0, v152
	v_exp_f32_e32 v152, v143
	v_rcp_f32_e32 v146, v146
	v_rcp_f32_e32 v147, v147
	v_pk_mul_f32 v[102:103], v[102:103], v[144:145]
	v_cvt_pk_f32_fp8_e32 v[144:145], v139
	v_med3_f32 v149, v149, s35, v177
	v_mul_f32_e32 v142, 0xbfb8aa3b, v142
	v_mul_f32_e32 v143, 0xbfb8aa3b, v149
	v_exp_f32_e32 v142, v142
	v_exp_f32_e32 v143, v143
	v_add_f32_e32 v149, 1.0, v152
	v_pk_add_f32 v[140:141], v[140:141], 1.0 op_sel_hi:[1,0]
	v_rcp_f32_e32 v148, v148
	v_rcp_f32_e32 v149, v149
	v_pk_mul_f32 v[140:141], v[146:147], v[140:141]
	v_cvt_pk_f32_fp8_sdwa v[138:139], v139 src0_sel:WORD_1
	v_pk_mul_f32 v[106:107], v[106:107], v[140:141]
	v_med3_f32 v141, v144, s35, v177
	v_pk_add_f32 v[142:143], v[142:143], 1.0 op_sel_hi:[1,0]
	v_mul_f32_e32 v141, 0xbfb8aa3b, v141
	v_pk_mul_f32 v[142:143], v[148:149], v[142:143]
	v_exp_f32_e32 v141, v141
	v_cvt_pk_f32_fp8_e32 v[150:151], v137
	v_cvt_pk_f32_fp8_sdwa v[136:137], v137 src0_sel:WORD_1
	v_pk_mul_f32 v[108:109], v[108:109], v[142:143]
	v_med3_f32 v143, v145, s35, v177
	v_med3_f32 v138, v138, s35, v177
	v_med3_f32 v139, v139, s35, v177
	v_mul_f32_e32 v143, 0xbfb8aa3b, v143
	v_mul_f32_e32 v138, 0xbfb8aa3b, v138
	v_mul_f32_e32 v139, 0xbfb8aa3b, v139
	v_add_f32_e32 v141, 1.0, v141
	v_exp_f32_e32 v143, v143
	v_exp_f32_e32 v138, v138
	v_exp_f32_e32 v139, v139
	v_rcp_f32_e32 v142, v141
	v_med3_f32 v140, v150, s35, v177
	v_med3_f32 v141, v151, s35, v177
	v_med3_f32 v136, v136, s35, v177
	v_med3_f32 v137, v137, s35, v177
	v_mul_f32_e32 v140, 0xbfb8aa3b, v140
	v_mul_f32_e32 v141, 0xbfb8aa3b, v141
	v_mul_f32_e32 v136, 0xbfb8aa3b, v136
	v_mul_f32_e32 v137, 0xbfb8aa3b, v137
	v_exp_f32_e32 v140, v140
	v_exp_f32_e32 v141, v141
	v_add_f32_e32 v143, 1.0, v143
	v_exp_f32_e32 v136, v136
	v_add_f32_e32 v138, 1.0, v138
	v_exp_f32_e32 v137, v137
	v_add_f32_e32 v139, 1.0, v139
	v_rcp_f32_e32 v143, v143
	v_rcp_f32_e32 v138, v138
	v_rcp_f32_e32 v139, v139
	v_pk_add_f32 v[136:137], v[136:137], 1.0 op_sel_hi:[1,0]
	v_pk_add_f32 v[140:141], v[140:141], 1.0 op_sel_hi:[1,0]
	v_pk_mul_f32 v[136:137], v[138:139], v[136:137]
	v_pk_mul_f32 v[140:141], v[142:143], v[140:141]
	v_pk_mul_f32 v[116:117], v[116:117], v[136:137]
	v_pk_mul_f32 v[114:115], v[114:115], v[140:141]
	s_nop 0
	s_waitcnt vmcnt(0)
	v_mov_b64_e32 v[162:163], v[220:221]
	v_mov_b64_e32 v[160:161], v[222:223]
	v_mov_b64_e32 v[178:179], v[224:225]
	v_mov_b64_e32 v[180:181], v[226:227]
	v_mov_b64_e32 v[158:159], v[228:229]
	v_mov_b64_e32 v[156:157], v[230:231]
	v_mov_b64_e32 v[154:155], v[232:233]
	v_mov_b64_e32 v[152:153], v[234:235]
	v_mov_b64_e32 v[150:151], v[236:237]
	v_mov_b64_e32 v[148:149], v[238:239]
	v_mov_b64_e32 v[146:147], v[240:241]
	v_mov_b64_e32 v[144:145], v[242:243]
	v_mov_b64_e32 v[142:143], v[244:245]
	v_mov_b64_e32 v[140:141], v[246:247]
	v_mov_b64_e32 v[138:139], v[248:249]
	v_mov_b64_e32 v[136:137], v[250:251]
	v_lshl_add_u32 v252, s23, 8, v214
	s_lshl_b32 s32, s60, 18
	v_add_u32_e32 v252, s32, v252
	global_load_dwordx2 v[220:221], v252, s[16:17]
	global_load_dwordx2 v[224:225], v252, s[16:17] offset:512
	global_load_dwordx2 v[228:229], v252, s[16:17] offset:1024
	global_load_dwordx2 v[232:233], v252, s[16:17] offset:1536
	global_load_dwordx2 v[236:237], v252, s[16:17] offset:2048
	global_load_dwordx2 v[240:241], v252, s[16:17] offset:2560
	global_load_dwordx2 v[244:245], v252, s[16:17] offset:3072
	global_load_dwordx2 v[248:249], v252, s[16:17] offset:3584
	v_cvt_pk_f32_fp8_e32 v[182:183], v162
	v_cvt_pk_f32_fp8_e32 v[188:189], v160
	v_cvt_pk_f32_fp8_sdwa v[184:185], v162 src0_sel:WORD_1
	v_cvt_pk_f32_fp8_sdwa v[190:191], v160 src0_sel:WORD_1
	v_med3_f32 v182, v182, s35, v177
	v_mul_f32_e32 v182, 0xbfb8aa3b, v182
	v_max_f32_e32 v134, v188, v188
	v_exp_f32_e32 v188, v182
	v_med3_f32 v134, v134, s35, v177
	v_mul_f32_e32 v134, 0xbfb8aa3b, v134
	v_med3_f32 v183, v183, s35, v177
	v_exp_f32_e32 v182, v134
	v_add_f32_e32 v134, 1.0, v188
	v_mul_f32_e32 v183, 0xbfb8aa3b, v183
	v_rcp_f32_e32 v188, v134
	v_max_f32_e32 v134, v189, v189
	v_exp_f32_e32 v189, v183
	v_med3_f32 v134, v134, s35, v177
	v_mul_f32_e32 v134, 0xbfb8aa3b, v134
	v_med3_f32 v184, v184, s35, v177
	v_exp_f32_e32 v183, v134
	v_add_f32_e32 v134, 1.0, v189
	v_mul_f32_e32 v184, 0xbfb8aa3b, v184
	v_rcp_f32_e32 v189, v134
	v_max_f32_e32 v134, v190, v190
	v_exp_f32_e32 v190, v184
	v_cvt_pk_f32_fp8_e32 v[186:187], v163
	v_med3_f32 v134, v134, s35, v177
	v_med3_f32 v185, v185, s35, v177
	v_mul_f32_e32 v134, 0xbfb8aa3b, v134
	v_mul_f32_e32 v185, 0xbfb8aa3b, v185
	v_pk_add_f32 v[182:183], v[182:183], 1.0 op_sel_hi:[1,0]
	v_exp_f32_e32 v184, v134
	v_add_f32_e32 v134, 1.0, v190
	v_max_f32_e32 v190, v191, v191
	v_exp_f32_e32 v191, v185
	v_pk_mul_f32 v[182:183], v[188:189], v[182:183]
	v_cvt_pk_f32_fp8_e32 v[192:193], v161
	v_pk_mul_f32 v[118:119], v[118:119], v[182:183]
	v_med3_f32 v182, v186, s35, v177
	v_med3_f32 v190, v190, s35, v177
	v_mul_f32_e32 v182, 0xbfb8aa3b, v182
	v_mul_f32_e32 v185, 0xbfb8aa3b, v190
	v_rcp_f32_e32 v190, v134
	v_add_f32_e32 v134, 1.0, v191
	v_exp_f32_e32 v183, v182
	v_exp_f32_e32 v185, v185
	v_rcp_f32_e32 v191, v134
	v_med3_f32 v134, v192, s35, v177
	v_mul_f32_e32 v134, 0xbfb8aa3b, v134
	v_exp_f32_e32 v182, v134
	v_add_f32_e32 v134, 1.0, v183
	v_pk_add_f32 v[184:185], v[184:185], 1.0 op_sel_hi:[1,0]
	v_med3_f32 v183, v187, s35, v177
	v_pk_mul_f32 v[184:185], v[190:191], v[184:185]
	v_mul_f32_e32 v183, 0xbfb8aa3b, v183
	v_pk_mul_f32 v[120:121], v[120:121], v[184:185]
	v_exp_f32_e32 v185, v183
	v_cvt_pk_f32_fp8_sdwa v[162:163], v163 src0_sel:WORD_1
	v_cvt_pk_f32_fp8_sdwa v[160:161], v161 src0_sel:WORD_1
	v_rcp_f32_e32 v184, v134
	v_med3_f32 v134, v193, s35, v177
	v_mul_f32_e32 v134, 0xbfb8aa3b, v134
	v_exp_f32_e32 v183, v134
	v_add_f32_e32 v134, 1.0, v185
	v_rcp_f32_e32 v185, v134
	v_max_f32_e32 v134, v160, v160
	v_med3_f32 v160, v162, s35, v177
	v_mul_f32_e32 v160, 0xbfb8aa3b, v160
	v_exp_f32_e32 v162, v160
	v_med3_f32 v134, v134, s35, v177
	v_mul_f32_e32 v134, 0xbfb8aa3b, v134
	v_exp_f32_e32 v160, v134
	v_add_f32_e32 v134, 1.0, v162
	v_med3_f32 v162, v163, s35, v177
	v_mul_f32_e32 v162, 0xbfb8aa3b, v162
	v_exp_f32_e32 v163, v162
	v_med3_f32 v161, v161, s35, v177
	v_mul_f32_e32 v161, 0xbfb8aa3b, v161
	v_exp_f32_e32 v161, v161
	v_rcp_f32_e32 v162, v134
	v_add_f32_e32 v134, 1.0, v163
	v_rcp_f32_e32 v163, v134
	v_pk_add_f32 v[160:161], v[160:161], 1.0 op_sel_hi:[1,0]
	v_pk_add_f32 v[182:183], v[182:183], 1.0 op_sel_hi:[1,0]
	v_cvt_pk_f32_fp8_sdwa v[186:187], v180 src0_sel:WORD_1
	v_pk_mul_f32 v[160:161], v[162:163], v[160:161]
	v_pk_mul_f32 v[182:183], v[184:185], v[182:183]
	v_pk_mul_f32 v[128:129], v[128:129], v[160:161]
	v_cvt_pk_f32_fp8_e32 v[160:161], v178
	v_cvt_pk_f32_fp8_e32 v[184:185], v180
	v_cvt_pk_f32_fp8_sdwa v[162:163], v178 src0_sel:WORD_1
	v_pk_mul_f32 v[126:127], v[126:127], v[182:183]
	v_med3_f32 v160, v160, s35, v177
	v_mul_f32_e32 v160, 0xbfb8aa3b, v160
	v_max_f32_e32 v134, v184, v184
	v_exp_f32_e32 v184, v160
	v_med3_f32 v134, v134, s35, v177
	v_mul_f32_e32 v134, 0xbfb8aa3b, v134
	v_med3_f32 v161, v161, s35, v177
	v_exp_f32_e32 v160, v134
	v_add_f32_e32 v134, 1.0, v184
	v_mul_f32_e32 v161, 0xbfb8aa3b, v161
	v_rcp_f32_e32 v184, v134
	v_max_f32_e32 v134, v185, v185
	v_exp_f32_e32 v185, v161
	v_med3_f32 v134, v134, s35, v177
	v_mul_f32_e32 v134, 0xbfb8aa3b, v134
	v_med3_f32 v162, v162, s35, v177
	v_exp_f32_e32 v161, v134
	v_add_f32_e32 v134, 1.0, v185
	v_mul_f32_e32 v162, 0xbfb8aa3b, v162
	v_rcp_f32_e32 v185, v134
	v_max_f32_e32 v134, v186, v186
	v_exp_f32_e32 v186, v162
	v_cvt_pk_f32_fp8_e32 v[182:183], v179
	v_med3_f32 v134, v134, s35, v177
	v_med3_f32 v163, v163, s35, v177
	v_mul_f32_e32 v134, 0xbfb8aa3b, v134
	v_mul_f32_e32 v163, 0xbfb8aa3b, v163
	v_pk_add_f32 v[160:161], v[160:161], 1.0 op_sel_hi:[1,0]
	v_exp_f32_e32 v162, v134
	v_add_f32_e32 v134, 1.0, v186
	v_max_f32_e32 v186, v187, v187
	v_exp_f32_e32 v187, v163
	v_pk_mul_f32 v[160:161], v[184:185], v[160:161]
	v_cvt_pk_f32_fp8_e32 v[188:189], v181
	v_pk_mul_f32 v[122:123], v[122:123], v[160:161]
	v_med3_f32 v160, v182, s35, v177
	v_med3_f32 v186, v186, s35, v177
	v_mul_f32_e32 v160, 0xbfb8aa3b, v160
	v_mul_f32_e32 v163, 0xbfb8aa3b, v186
	v_rcp_f32_e32 v186, v134
	v_add_f32_e32 v134, 1.0, v187
	v_exp_f32_e32 v161, v160
	v_exp_f32_e32 v163, v163
	v_rcp_f32_e32 v187, v134
	v_med3_f32 v134, v188, s35, v177
	v_mul_f32_e32 v134, 0xbfb8aa3b, v134
	v_exp_f32_e32 v160, v134
	v_add_f32_e32 v134, 1.0, v161
	v_cvt_pk_f32_fp8_sdwa v[178:179], v179 src0_sel:WORD_1
	v_pk_add_f32 v[162:163], v[162:163], 1.0 op_sel_hi:[1,0]
	v_med3_f32 v161, v183, s35, v177
	v_pk_mul_f32 v[162:163], v[186:187], v[162:163]
	v_mul_f32_e32 v161, 0xbfb8aa3b, v161
	v_pk_mul_f32 v[124:125], v[124:125], v[162:163]
	v_exp_f32_e32 v163, v161
	v_cvt_pk_f32_fp8_sdwa v[180:181], v181 src0_sel:WORD_1
	v_rcp_f32_e32 v162, v134
	v_med3_f32 v134, v189, s35, v177
	v_mul_f32_e32 v134, 0xbfb8aa3b, v134
	v_med3_f32 v178, v178, s35, v177
	v_exp_f32_e32 v161, v134
	v_add_f32_e32 v134, 1.0, v163
	v_mul_f32_e32 v178, 0xbfb8aa3b, v178
	v_rcp_f32_e32 v163, v134
	v_max_f32_e32 v134, v180, v180
	v_exp_f32_e32 v180, v178
	v_med3_f32 v134, v134, s35, v177
	v_med3_f32 v179, v179, s35, v177
	v_mul_f32_e32 v134, 0xbfb8aa3b, v134
	v_mul_f32_e32 v179, 0xbfb8aa3b, v179
	v_exp_f32_e32 v178, v134
	v_add_f32_e32 v134, 1.0, v180
	v_max_f32_e32 v180, v181, v181
	v_exp_f32_e32 v181, v179
	v_med3_f32 v180, v180, s35, v177
	v_mul_f32_e32 v179, 0xbfb8aa3b, v180
	v_exp_f32_e32 v179, v179
	v_rcp_f32_e32 v180, v134
	v_add_f32_e32 v134, 1.0, v181
	v_pk_add_f32 v[160:161], v[160:161], 1.0 op_sel_hi:[1,0]
	v_rcp_f32_e32 v181, v134
	v_pk_mul_f32 v[160:161], v[162:163], v[160:161]
	v_pk_add_f32 v[178:179], v[178:179], 1.0 op_sel_hi:[1,0]
	v_pk_mul_f32 v[110:111], v[110:111], v[160:161]
	v_cvt_pk_f32_fp8_e32 v[160:161], v158
	v_pk_mul_f32 v[162:163], v[180:181], v[178:179]
	v_cvt_pk_f32_fp8_e32 v[180:181], v156
	v_pk_mul_f32 v[112:113], v[112:113], v[162:163]
	v_med3_f32 v160, v160, s35, v177
	v_mul_f32_e32 v160, 0xbfb8aa3b, v160
	v_max_f32_e32 v134, v180, v180
	v_exp_f32_e32 v180, v160
	v_med3_f32 v134, v134, s35, v177
	v_cvt_pk_f32_fp8_sdwa v[162:163], v158 src0_sel:WORD_1
	v_mul_f32_e32 v134, 0xbfb8aa3b, v134
	v_med3_f32 v161, v161, s35, v177
	v_exp_f32_e32 v160, v134
	v_add_f32_e32 v134, 1.0, v180
	v_mul_f32_e32 v161, 0xbfb8aa3b, v161
	v_rcp_f32_e32 v180, v134
	v_max_f32_e32 v134, v181, v181
	v_exp_f32_e32 v181, v161
	v_cvt_pk_f32_fp8_sdwa v[182:183], v156 src0_sel:WORD_1
	v_med3_f32 v134, v134, s35, v177
	v_mul_f32_e32 v134, 0xbfb8aa3b, v134
	v_med3_f32 v162, v162, s35, v177
	v_exp_f32_e32 v161, v134
	v_add_f32_e32 v134, 1.0, v181
	v_mul_f32_e32 v162, 0xbfb8aa3b, v162
	v_rcp_f32_e32 v181, v134
	v_max_f32_e32 v134, v182, v182
	v_exp_f32_e32 v182, v162
	v_cvt_pk_f32_fp8_e32 v[178:179], v159
	v_med3_f32 v134, v134, s35, v177
	v_med3_f32 v163, v163, s35, v177
	v_mul_f32_e32 v134, 0xbfb8aa3b, v134
	v_mul_f32_e32 v163, 0xbfb8aa3b, v163
	v_pk_add_f32 v[160:161], v[160:161], 1.0 op_sel_hi:[1,0]
	v_exp_f32_e32 v162, v134
	v_add_f32_e32 v134, 1.0, v182
	v_max_f32_e32 v182, v183, v183
	v_exp_f32_e32 v183, v163
	v_pk_mul_f32 v[160:161], v[180:181], v[160:161]
	v_cvt_pk_f32_fp8_e32 v[184:185], v157
	v_pk_mul_f32 v[98:99], v[98:99], v[160:161]
	v_med3_f32 v160, v178, s35, v177
	v_med3_f32 v182, v182, s35, v177
	v_mul_f32_e32 v160, 0xbfb8aa3b, v160
	v_mul_f32_e32 v163, 0xbfb8aa3b, v182
	v_rcp_f32_e32 v182, v134
	v_add_f32_e32 v134, 1.0, v183
	v_exp_f32_e32 v161, v160
	v_exp_f32_e32 v163, v163
	v_rcp_f32_e32 v183, v134
	v_med3_f32 v134, v184, s35, v177
	v_mul_f32_e32 v134, 0xbfb8aa3b, v134
	v_exp_f32_e32 v160, v134
	v_add_f32_e32 v134, 1.0, v161
	v_pk_add_f32 v[162:163], v[162:163], 1.0 op_sel_hi:[1,0]
	v_med3_f32 v161, v179, s35, v177
	v_pk_mul_f32 v[162:163], v[182:183], v[162:163]
	v_mul_f32_e32 v161, 0xbfb8aa3b, v161
	v_pk_mul_f32 v[100:101], v[100:101], v[162:163]
	v_exp_f32_e32 v163, v161
	v_cvt_pk_f32_fp8_sdwa v[158:159], v159 src0_sel:WORD_1
	v_cvt_pk_f32_fp8_sdwa v[156:157], v157 src0_sel:WORD_1
	v_rcp_f32_e32 v162, v134
	v_med3_f32 v134, v185, s35, v177
	v_mul_f32_e32 v134, 0xbfb8aa3b, v134
	v_exp_f32_e32 v161, v134
	v_add_f32_e32 v134, 1.0, v163
	v_rcp_f32_e32 v163, v134
	v_max_f32_e32 v134, v156, v156
	v_med3_f32 v156, v158, s35, v177
	v_mul_f32_e32 v156, 0xbfb8aa3b, v156
	v_exp_f32_e32 v158, v156
	v_med3_f32 v134, v134, s35, v177
	v_mul_f32_e32 v134, 0xbfb8aa3b, v134
	v_exp_f32_e32 v156, v134
	v_add_f32_e32 v134, 1.0, v158
	v_med3_f32 v158, v159, s35, v177
	v_mul_f32_e32 v158, 0xbfb8aa3b, v158
	v_exp_f32_e32 v159, v158
	v_med3_f32 v157, v157, s35, v177
	v_mul_f32_e32 v157, 0xbfb8aa3b, v157
	v_exp_f32_e32 v157, v157
	v_rcp_f32_e32 v158, v134
	v_add_f32_e32 v134, 1.0, v159
	v_rcp_f32_e32 v159, v134
	v_pk_add_f32 v[156:157], v[156:157], 1.0 op_sel_hi:[1,0]
	v_pk_add_f32 v[160:161], v[160:161], 1.0 op_sel_hi:[1,0]
	v_cvt_pk_f32_fp8_sdwa v[178:179], v152 src0_sel:WORD_1
	v_pk_mul_f32 v[156:157], v[158:159], v[156:157]
	v_pk_mul_f32 v[160:161], v[162:163], v[160:161]
	v_pk_mul_f32 v[88:89], v[88:89], v[156:157]
	v_cvt_pk_f32_fp8_e32 v[156:157], v154
	v_cvt_pk_f32_fp8_e32 v[162:163], v152
	v_cvt_pk_f32_fp8_sdwa v[158:159], v154 src0_sel:WORD_1
	v_pk_mul_f32 v[86:87], v[86:87], v[160:161]
	v_med3_f32 v156, v156, s35, v177
	v_mul_f32_e32 v156, 0xbfb8aa3b, v156
	v_max_f32_e32 v134, v162, v162
	v_exp_f32_e32 v162, v156
	v_med3_f32 v134, v134, s35, v177
	v_mul_f32_e32 v134, 0xbfb8aa3b, v134
	v_med3_f32 v157, v157, s35, v177
	v_exp_f32_e32 v156, v134
	v_add_f32_e32 v134, 1.0, v162
	v_mul_f32_e32 v157, 0xbfb8aa3b, v157
	v_rcp_f32_e32 v162, v134
	v_max_f32_e32 v134, v163, v163
	v_exp_f32_e32 v163, v157
	v_med3_f32 v134, v134, s35, v177
	v_mul_f32_e32 v134, 0xbfb8aa3b, v134
	v_med3_f32 v158, v158, s35, v177
	v_exp_f32_e32 v157, v134
	v_add_f32_e32 v134, 1.0, v163
	v_mul_f32_e32 v158, 0xbfb8aa3b, v158
	v_rcp_f32_e32 v163, v134
	v_max_f32_e32 v134, v178, v178
	v_exp_f32_e32 v178, v158
	v_cvt_pk_f32_fp8_e32 v[160:161], v155
	v_med3_f32 v134, v134, s35, v177
	v_med3_f32 v159, v159, s35, v177
	v_mul_f32_e32 v134, 0xbfb8aa3b, v134
	v_mul_f32_e32 v159, 0xbfb8aa3b, v159
	v_pk_add_f32 v[156:157], v[156:157], 1.0 op_sel_hi:[1,0]
	v_exp_f32_e32 v158, v134
	v_add_f32_e32 v134, 1.0, v178
	v_max_f32_e32 v178, v179, v179
	v_exp_f32_e32 v179, v159
	v_pk_mul_f32 v[156:157], v[162:163], v[156:157]
	v_cvt_pk_f32_fp8_e32 v[180:181], v153
	v_pk_mul_f32 v[70:71], v[70:71], v[156:157]
	v_med3_f32 v156, v160, s35, v177
	v_med3_f32 v178, v178, s35, v177
	v_mul_f32_e32 v156, 0xbfb8aa3b, v156
	v_mul_f32_e32 v159, 0xbfb8aa3b, v178
	v_rcp_f32_e32 v178, v134
	v_add_f32_e32 v134, 1.0, v179
	v_exp_f32_e32 v157, v156
	v_exp_f32_e32 v159, v159
	v_rcp_f32_e32 v179, v134
	v_med3_f32 v134, v180, s35, v177
	v_mul_f32_e32 v134, 0xbfb8aa3b, v134
	v_exp_f32_e32 v156, v134
	v_add_f32_e32 v134, 1.0, v157
	v_pk_add_f32 v[158:159], v[158:159], 1.0 op_sel_hi:[1,0]
	v_med3_f32 v157, v161, s35, v177
	v_pk_mul_f32 v[158:159], v[178:179], v[158:159]
	v_mul_f32_e32 v157, 0xbfb8aa3b, v157
	v_pk_mul_f32 v[72:73], v[72:73], v[158:159]
	v_exp_f32_e32 v159, v157
	v_cvt_pk_f32_fp8_sdwa v[154:155], v155 src0_sel:WORD_1
	v_cvt_pk_f32_fp8_sdwa v[152:153], v153 src0_sel:WORD_1
	v_rcp_f32_e32 v158, v134
	v_med3_f32 v134, v181, s35, v177
	v_mul_f32_e32 v134, 0xbfb8aa3b, v134
	v_exp_f32_e32 v157, v134
	v_add_f32_e32 v134, 1.0, v159
	v_rcp_f32_e32 v159, v134
	v_max_f32_e32 v134, v152, v152
	v_med3_f32 v152, v154, s35, v177
	v_mul_f32_e32 v152, 0xbfb8aa3b, v152
	v_exp_f32_e32 v154, v152
	v_med3_f32 v134, v134, s35, v177
	v_mul_f32_e32 v134, 0xbfb8aa3b, v134
	v_exp_f32_e32 v152, v134
	v_add_f32_e32 v134, 1.0, v154
	v_med3_f32 v154, v155, s35, v177
	v_mul_f32_e32 v154, 0xbfb8aa3b, v154
	v_exp_f32_e32 v155, v154
	v_med3_f32 v153, v153, s35, v177
	v_mul_f32_e32 v153, 0xbfb8aa3b, v153
	v_exp_f32_e32 v153, v153
	v_rcp_f32_e32 v154, v134
	v_add_f32_e32 v134, 1.0, v155
	v_rcp_f32_e32 v155, v134
	v_pk_add_f32 v[152:153], v[152:153], 1.0 op_sel_hi:[1,0]
	v_pk_add_f32 v[156:157], v[156:157], 1.0 op_sel_hi:[1,0]
	v_cvt_pk_f32_fp8_sdwa v[160:161], v148 src0_sel:WORD_1
	v_pk_mul_f32 v[152:153], v[154:155], v[152:153]
	v_pk_mul_f32 v[156:157], v[158:159], v[156:157]
	v_pk_mul_f32 v[60:61], v[60:61], v[152:153]
	v_cvt_pk_f32_fp8_e32 v[152:153], v150
	v_cvt_pk_f32_fp8_e32 v[158:159], v148
	v_cvt_pk_f32_fp8_sdwa v[154:155], v150 src0_sel:WORD_1
	v_pk_mul_f32 v[58:59], v[58:59], v[156:157]
	v_med3_f32 v152, v152, s35, v177
	v_mul_f32_e32 v152, 0xbfb8aa3b, v152
	v_max_f32_e32 v134, v158, v158
	v_exp_f32_e32 v158, v152
	v_med3_f32 v134, v134, s35, v177
	v_mul_f32_e32 v134, 0xbfb8aa3b, v134
	v_med3_f32 v153, v153, s35, v177
	v_exp_f32_e32 v152, v134
	v_add_f32_e32 v134, 1.0, v158
	v_mul_f32_e32 v153, 0xbfb8aa3b, v153
	v_rcp_f32_e32 v158, v134
	v_max_f32_e32 v134, v159, v159
	v_exp_f32_e32 v159, v153
	v_med3_f32 v134, v134, s35, v177
	v_mul_f32_e32 v134, 0xbfb8aa3b, v134
	v_med3_f32 v154, v154, s35, v177
	v_exp_f32_e32 v153, v134
	v_add_f32_e32 v134, 1.0, v159
	v_mul_f32_e32 v154, 0xbfb8aa3b, v154
	v_rcp_f32_e32 v159, v134
	v_max_f32_e32 v134, v160, v160
	v_exp_f32_e32 v160, v154
	v_cvt_pk_f32_fp8_e32 v[156:157], v151
	v_med3_f32 v134, v134, s35, v177
	v_med3_f32 v155, v155, s35, v177
	v_mul_f32_e32 v134, 0xbfb8aa3b, v134
	v_mul_f32_e32 v155, 0xbfb8aa3b, v155
	v_pk_add_f32 v[152:153], v[152:153], 1.0 op_sel_hi:[1,0]
	v_exp_f32_e32 v154, v134
	v_add_f32_e32 v134, 1.0, v160
	v_max_f32_e32 v160, v161, v161
	v_exp_f32_e32 v161, v155
	v_pk_mul_f32 v[152:153], v[158:159], v[152:153]
	v_cvt_pk_f32_fp8_e32 v[162:163], v149
	v_pk_mul_f32 v[46:47], v[46:47], v[152:153]
	v_med3_f32 v152, v156, s35, v177
	v_med3_f32 v160, v160, s35, v177
	v_mul_f32_e32 v152, 0xbfb8aa3b, v152
	v_mul_f32_e32 v155, 0xbfb8aa3b, v160
	v_rcp_f32_e32 v160, v134
	v_add_f32_e32 v134, 1.0, v161
	v_exp_f32_e32 v153, v152
	v_exp_f32_e32 v155, v155
	v_rcp_f32_e32 v161, v134
	v_med3_f32 v134, v162, s35, v177
	v_mul_f32_e32 v134, 0xbfb8aa3b, v134
	v_exp_f32_e32 v152, v134
	v_add_f32_e32 v134, 1.0, v153
	v_pk_add_f32 v[154:155], v[154:155], 1.0 op_sel_hi:[1,0]
	v_med3_f32 v153, v157, s35, v177
	v_pk_mul_f32 v[154:155], v[160:161], v[154:155]
	v_mul_f32_e32 v153, 0xbfb8aa3b, v153
	v_pk_mul_f32 v[48:49], v[48:49], v[154:155]
	v_exp_f32_e32 v155, v153
	v_cvt_pk_f32_fp8_sdwa v[150:151], v151 src0_sel:WORD_1
	v_cvt_pk_f32_fp8_sdwa v[148:149], v149 src0_sel:WORD_1
	v_rcp_f32_e32 v154, v134
	v_med3_f32 v134, v163, s35, v177
	v_mul_f32_e32 v134, 0xbfb8aa3b, v134
	v_exp_f32_e32 v153, v134
	v_add_f32_e32 v134, 1.0, v155
	v_rcp_f32_e32 v155, v134
	v_max_f32_e32 v134, v148, v148
	v_med3_f32 v148, v150, s35, v177
	v_mul_f32_e32 v148, 0xbfb8aa3b, v148
	v_exp_f32_e32 v150, v148
	v_med3_f32 v134, v134, s35, v177
	v_mul_f32_e32 v134, 0xbfb8aa3b, v134
	v_exp_f32_e32 v148, v134
	v_add_f32_e32 v134, 1.0, v150
	v_med3_f32 v150, v151, s35, v177
	v_mul_f32_e32 v150, 0xbfb8aa3b, v150
	v_exp_f32_e32 v151, v150
	v_med3_f32 v149, v149, s35, v177
	v_mul_f32_e32 v149, 0xbfb8aa3b, v149
	v_exp_f32_e32 v149, v149
	v_rcp_f32_e32 v150, v134
	v_add_f32_e32 v134, 1.0, v151
	v_rcp_f32_e32 v151, v134
	v_pk_add_f32 v[148:149], v[148:149], 1.0 op_sel_hi:[1,0]
	v_pk_add_f32 v[152:153], v[152:153], 1.0 op_sel_hi:[1,0]
	v_cvt_pk_f32_fp8_sdwa v[156:157], v144 src0_sel:WORD_1
	v_pk_mul_f32 v[148:149], v[150:151], v[148:149]
	v_pk_mul_f32 v[152:153], v[154:155], v[152:153]
	v_pk_mul_f32 v[36:37], v[36:37], v[148:149]
	v_cvt_pk_f32_fp8_e32 v[148:149], v146
	v_cvt_pk_f32_fp8_e32 v[154:155], v144
	v_cvt_pk_f32_fp8_sdwa v[150:151], v146 src0_sel:WORD_1
	v_pk_mul_f32 v[34:35], v[34:35], v[152:153]
	v_med3_f32 v148, v148, s35, v177
	v_mul_f32_e32 v148, 0xbfb8aa3b, v148
	v_max_f32_e32 v134, v154, v154
	v_exp_f32_e32 v154, v148
	v_med3_f32 v134, v134, s35, v177
	v_mul_f32_e32 v134, 0xbfb8aa3b, v134
	v_med3_f32 v149, v149, s35, v177
	v_exp_f32_e32 v148, v134
	v_add_f32_e32 v134, 1.0, v154
	v_mul_f32_e32 v149, 0xbfb8aa3b, v149
	v_rcp_f32_e32 v154, v134
	v_max_f32_e32 v134, v155, v155
	v_exp_f32_e32 v155, v149
	v_med3_f32 v134, v134, s35, v177
	v_mul_f32_e32 v134, 0xbfb8aa3b, v134
	v_med3_f32 v150, v150, s35, v177
	v_exp_f32_e32 v149, v134
	v_add_f32_e32 v134, 1.0, v155
	v_mul_f32_e32 v150, 0xbfb8aa3b, v150
	v_rcp_f32_e32 v155, v134
	v_max_f32_e32 v134, v156, v156
	v_exp_f32_e32 v156, v150
	v_cvt_pk_f32_fp8_e32 v[152:153], v147
	v_med3_f32 v134, v134, s35, v177
	v_med3_f32 v151, v151, s35, v177
	v_mul_f32_e32 v134, 0xbfb8aa3b, v134
	v_mul_f32_e32 v151, 0xbfb8aa3b, v151
	v_pk_add_f32 v[148:149], v[148:149], 1.0 op_sel_hi:[1,0]
	v_exp_f32_e32 v150, v134
	v_add_f32_e32 v134, 1.0, v156
	v_max_f32_e32 v156, v157, v157
	v_exp_f32_e32 v157, v151
	v_pk_mul_f32 v[148:149], v[154:155], v[148:149]
	v_cvt_pk_f32_fp8_e32 v[158:159], v145
	v_pk_mul_f32 v[22:23], v[22:23], v[148:149]
	v_med3_f32 v148, v152, s35, v177
	v_med3_f32 v156, v156, s35, v177
	v_mul_f32_e32 v148, 0xbfb8aa3b, v148
	v_mul_f32_e32 v151, 0xbfb8aa3b, v156
	v_rcp_f32_e32 v156, v134
	v_add_f32_e32 v134, 1.0, v157
	v_exp_f32_e32 v149, v148
	v_exp_f32_e32 v151, v151
	v_rcp_f32_e32 v157, v134
	v_med3_f32 v134, v158, s35, v177
	v_mul_f32_e32 v134, 0xbfb8aa3b, v134
	v_exp_f32_e32 v148, v134
	v_add_f32_e32 v134, 1.0, v149
	v_pk_add_f32 v[150:151], v[150:151], 1.0 op_sel_hi:[1,0]
	v_med3_f32 v149, v153, s35, v177
	v_pk_mul_f32 v[150:151], v[156:157], v[150:151]
	v_mul_f32_e32 v149, 0xbfb8aa3b, v149
	v_pk_mul_f32 v[24:25], v[24:25], v[150:151]
	v_exp_f32_e32 v151, v149
	v_cvt_pk_f32_fp8_sdwa v[146:147], v147 src0_sel:WORD_1
	v_cvt_pk_f32_fp8_sdwa v[144:145], v145 src0_sel:WORD_1
	v_rcp_f32_e32 v150, v134
	v_med3_f32 v134, v159, s35, v177
	v_mul_f32_e32 v134, 0xbfb8aa3b, v134
	v_exp_f32_e32 v149, v134
	v_add_f32_e32 v134, 1.0, v151
	v_rcp_f32_e32 v151, v134
	v_max_f32_e32 v134, v144, v144
	v_med3_f32 v144, v146, s35, v177
	v_mul_f32_e32 v144, 0xbfb8aa3b, v144
	v_exp_f32_e32 v146, v144
	v_med3_f32 v134, v134, s35, v177
	v_mul_f32_e32 v134, 0xbfb8aa3b, v134
	v_exp_f32_e32 v144, v134
	v_add_f32_e32 v134, 1.0, v146
	v_med3_f32 v146, v147, s35, v177
	v_mul_f32_e32 v146, 0xbfb8aa3b, v146
	v_exp_f32_e32 v147, v146
	v_med3_f32 v145, v145, s35, v177
	v_mul_f32_e32 v145, 0xbfb8aa3b, v145
	v_exp_f32_e32 v145, v145
	v_rcp_f32_e32 v146, v134
	v_add_f32_e32 v134, 1.0, v147
	v_rcp_f32_e32 v147, v134
	v_pk_add_f32 v[144:145], v[144:145], 1.0 op_sel_hi:[1,0]
	v_pk_add_f32 v[148:149], v[148:149], 1.0 op_sel_hi:[1,0]
	v_cvt_pk_f32_fp8_sdwa v[152:153], v140 src0_sel:WORD_1
	v_pk_mul_f32 v[144:145], v[146:147], v[144:145]
	v_pk_mul_f32 v[148:149], v[150:151], v[148:149]
	v_pk_mul_f32 v[20:21], v[20:21], v[144:145]
	v_cvt_pk_f32_fp8_e32 v[144:145], v142
	v_cvt_pk_f32_fp8_e32 v[150:151], v140
	v_cvt_pk_f32_fp8_sdwa v[146:147], v142 src0_sel:WORD_1
	v_pk_mul_f32 v[18:19], v[18:19], v[148:149]
	v_med3_f32 v144, v144, s35, v177
	v_mul_f32_e32 v144, 0xbfb8aa3b, v144
	v_max_f32_e32 v134, v150, v150
	v_exp_f32_e32 v150, v144
	v_med3_f32 v134, v134, s35, v177
	v_mul_f32_e32 v134, 0xbfb8aa3b, v134
	v_med3_f32 v145, v145, s35, v177
	v_exp_f32_e32 v144, v134
	v_add_f32_e32 v134, 1.0, v150
	v_mul_f32_e32 v145, 0xbfb8aa3b, v145
	v_rcp_f32_e32 v150, v134
	v_max_f32_e32 v134, v151, v151
	v_exp_f32_e32 v151, v145
	v_med3_f32 v134, v134, s35, v177
	v_mul_f32_e32 v134, 0xbfb8aa3b, v134
	v_med3_f32 v146, v146, s35, v177
	v_exp_f32_e32 v145, v134
	v_add_f32_e32 v134, 1.0, v151
	v_mul_f32_e32 v146, 0xbfb8aa3b, v146
	v_rcp_f32_e32 v151, v134
	v_max_f32_e32 v134, v152, v152
	v_exp_f32_e32 v152, v146
	v_cvt_pk_f32_fp8_e32 v[148:149], v143
	v_med3_f32 v134, v134, s35, v177
	v_med3_f32 v147, v147, s35, v177
	v_mul_f32_e32 v134, 0xbfb8aa3b, v134
	v_mul_f32_e32 v147, 0xbfb8aa3b, v147
	v_pk_add_f32 v[144:145], v[144:145], 1.0 op_sel_hi:[1,0]
	v_exp_f32_e32 v146, v134
	v_add_f32_e32 v134, 1.0, v152
	v_max_f32_e32 v152, v153, v153
	v_exp_f32_e32 v153, v147
	v_pk_mul_f32 v[144:145], v[150:151], v[144:145]
	v_cvt_pk_f32_fp8_e32 v[154:155], v141
	v_pk_mul_f32 v[14:15], v[14:15], v[144:145]
	v_med3_f32 v144, v148, s35, v177
	v_med3_f32 v152, v152, s35, v177
	v_mul_f32_e32 v144, 0xbfb8aa3b, v144
	v_mul_f32_e32 v147, 0xbfb8aa3b, v152
	v_rcp_f32_e32 v152, v134
	v_add_f32_e32 v134, 1.0, v153
	v_exp_f32_e32 v145, v144
	v_exp_f32_e32 v147, v147
	v_rcp_f32_e32 v153, v134
	v_med3_f32 v134, v154, s35, v177
	v_mul_f32_e32 v134, 0xbfb8aa3b, v134
	v_exp_f32_e32 v144, v134
	v_add_f32_e32 v134, 1.0, v145
	v_pk_add_f32 v[146:147], v[146:147], 1.0 op_sel_hi:[1,0]
	v_med3_f32 v145, v149, s35, v177
	v_pk_mul_f32 v[146:147], v[152:153], v[146:147]
	v_mul_f32_e32 v145, 0xbfb8aa3b, v145
	v_pk_mul_f32 v[16:17], v[16:17], v[146:147]
	v_exp_f32_e32 v147, v145
	v_cvt_pk_f32_fp8_sdwa v[142:143], v143 src0_sel:WORD_1
	v_cvt_pk_f32_fp8_sdwa v[140:141], v141 src0_sel:WORD_1
	v_rcp_f32_e32 v146, v134
	v_med3_f32 v134, v155, s35, v177
	v_mul_f32_e32 v134, 0xbfb8aa3b, v134
	v_exp_f32_e32 v145, v134
	v_add_f32_e32 v134, 1.0, v147
	v_rcp_f32_e32 v147, v134
	v_max_f32_e32 v134, v140, v140
	v_med3_f32 v140, v142, s35, v177
	v_mul_f32_e32 v140, 0xbfb8aa3b, v140
	v_exp_f32_e32 v142, v140
	v_med3_f32 v134, v134, s35, v177
	v_mul_f32_e32 v134, 0xbfb8aa3b, v134
	v_exp_f32_e32 v140, v134
	v_add_f32_e32 v134, 1.0, v142
	v_med3_f32 v142, v143, s35, v177
	v_mul_f32_e32 v142, 0xbfb8aa3b, v142
	v_exp_f32_e32 v143, v142
	v_med3_f32 v141, v141, s35, v177
	v_mul_f32_e32 v141, 0xbfb8aa3b, v141
	v_exp_f32_e32 v141, v141
	v_rcp_f32_e32 v142, v134
	v_add_f32_e32 v134, 1.0, v143
	v_rcp_f32_e32 v143, v134
	v_pk_add_f32 v[140:141], v[140:141], 1.0 op_sel_hi:[1,0]
	v_pk_add_f32 v[144:145], v[144:145], 1.0 op_sel_hi:[1,0]
	s_waitcnt vmcnt(0)
	v_cvt_pk_f32_fp8_sdwa v[148:149], v136 src0_sel:WORD_1
	v_pk_mul_f32 v[140:141], v[142:143], v[140:141]
	v_pk_mul_f32 v[144:145], v[146:147], v[144:145]
	v_pk_mul_f32 v[12:13], v[12:13], v[140:141]
	v_cvt_pk_f32_fp8_e32 v[140:141], v138
	v_cvt_pk_f32_fp8_e32 v[146:147], v136
	v_cvt_pk_f32_fp8_sdwa v[142:143], v138 src0_sel:WORD_1
	v_pk_mul_f32 v[10:11], v[10:11], v[144:145]
	v_med3_f32 v140, v140, s35, v177
	v_mul_f32_e32 v140, 0xbfb8aa3b, v140
	v_max_f32_e32 v134, v146, v146
	v_exp_f32_e32 v146, v140
	v_med3_f32 v134, v134, s35, v177
	v_mul_f32_e32 v134, 0xbfb8aa3b, v134
	v_med3_f32 v141, v141, s35, v177
	v_exp_f32_e32 v140, v134
	v_add_f32_e32 v134, 1.0, v146
	v_mul_f32_e32 v141, 0xbfb8aa3b, v141
	v_rcp_f32_e32 v146, v134
	v_max_f32_e32 v134, v147, v147
	v_exp_f32_e32 v147, v141
	v_med3_f32 v134, v134, s35, v177
	v_mul_f32_e32 v134, 0xbfb8aa3b, v134
	v_med3_f32 v142, v142, s35, v177
	v_exp_f32_e32 v141, v134
	v_add_f32_e32 v134, 1.0, v147
	v_mul_f32_e32 v142, 0xbfb8aa3b, v142
	v_rcp_f32_e32 v147, v134
	v_max_f32_e32 v134, v148, v148
	v_exp_f32_e32 v148, v142
	v_cvt_pk_f32_fp8_e32 v[144:145], v139
	v_med3_f32 v134, v134, s35, v177
	v_med3_f32 v143, v143, s35, v177
	v_mul_f32_e32 v134, 0xbfb8aa3b, v134
	v_mul_f32_e32 v143, 0xbfb8aa3b, v143
	v_pk_add_f32 v[140:141], v[140:141], 1.0 op_sel_hi:[1,0]
	v_exp_f32_e32 v142, v134
	v_add_f32_e32 v134, 1.0, v148
	v_max_f32_e32 v148, v149, v149
	v_exp_f32_e32 v149, v143
	v_pk_mul_f32 v[140:141], v[146:147], v[140:141]
	v_cvt_pk_f32_fp8_e32 v[150:151], v137
	v_pk_mul_f32 v[6:7], v[6:7], v[140:141]
	v_med3_f32 v140, v144, s35, v177
	v_med3_f32 v148, v148, s35, v177
	v_mul_f32_e32 v140, 0xbfb8aa3b, v140
	v_mul_f32_e32 v143, 0xbfb8aa3b, v148
	v_rcp_f32_e32 v148, v134
	v_add_f32_e32 v134, 1.0, v149
	v_exp_f32_e32 v141, v140
	v_exp_f32_e32 v143, v143
	v_rcp_f32_e32 v149, v134
	v_med3_f32 v134, v150, s35, v177
	v_mul_f32_e32 v134, 0xbfb8aa3b, v134
	v_exp_f32_e32 v140, v134
	v_add_f32_e32 v134, 1.0, v141
	v_pk_add_f32 v[142:143], v[142:143], 1.0 op_sel_hi:[1,0]
	v_med3_f32 v141, v145, s35, v177
	v_pk_mul_f32 v[142:143], v[148:149], v[142:143]
	v_mul_f32_e32 v141, 0xbfb8aa3b, v141
	v_pk_mul_f32 v[8:9], v[8:9], v[142:143]
	v_exp_f32_e32 v143, v141
	v_cvt_pk_f32_fp8_sdwa v[138:139], v139 src0_sel:WORD_1
	v_cvt_pk_f32_fp8_sdwa v[136:137], v137 src0_sel:WORD_1
	v_rcp_f32_e32 v142, v134
	v_med3_f32 v134, v151, s35, v177
	v_mul_f32_e32 v134, 0xbfb8aa3b, v134
	v_exp_f32_e32 v141, v134
	v_add_f32_e32 v134, 1.0, v143
	v_rcp_f32_e32 v143, v134
	v_max_f32_e32 v134, v136, v136
	v_med3_f32 v136, v138, s35, v177
	v_mul_f32_e32 v136, 0xbfb8aa3b, v136
	v_exp_f32_e32 v138, v136
	v_med3_f32 v134, v134, s35, v177
	v_mul_f32_e32 v134, 0xbfb8aa3b, v134
	v_exp_f32_e32 v136, v134
	v_add_f32_e32 v134, 1.0, v138
	v_med3_f32 v138, v139, s35, v177
	v_mul_f32_e32 v138, 0xbfb8aa3b, v138
	v_exp_f32_e32 v139, v138
	v_med3_f32 v137, v137, s35, v177
	v_mul_f32_e32 v137, 0xbfb8aa3b, v137
	v_exp_f32_e32 v137, v137
	v_rcp_f32_e32 v138, v134
	v_add_f32_e32 v134, 1.0, v139
	v_rcp_f32_e32 v139, v134
	v_pk_add_f32 v[136:137], v[136:137], 1.0 op_sel_hi:[1,0]
	v_pk_add_f32 v[140:141], v[140:141], 1.0 op_sel_hi:[1,0]
	v_pk_mul_f32 v[136:137], v[138:139], v[136:137]
	v_pk_mul_f32 v[140:141], v[142:143], v[140:141]
	v_pk_mul_f32 v[4:5], v[4:5], v[136:137]
	v_pk_mul_f32 v[2:3], v[2:3], v[140:141]
	s_nop 0
